# gdnprep conv: k / v segment rows touched while the q segment rows load (their later loads hit L1/L2)
# baseline (speedup 1.0000x reference)
; DI void gdn_prep_unit(const Params& p, int U, char* lds) {
;     ...
;     for (int X = 0; X < 3; ++X) {
;       const int col = 1536 + 512 * X + h * 128 + 2 * lane, cb = 512 * X + h * 128 + 2 * lane;
;       float w0[4], w1[4];
; #pragma unroll
;       for (int j = 0; j < 4; ++j) { w0[j] = p.conv_w[j * 1536 + cb]; w1[j] = p.conv_w[j * 1536 + cb + 1]; }
;       bf16_t* dst = X == 0 ? q_s : (X == 1 ? k_s : v_s);
;       const int i0 = 16 * wid;
;       unsigned raw[19];
;       {
;         const unsigned* pr[19];
; #pragma unroll
;         for (int j = 0; j < 19; ++j) { const int rr = i0 - 3 + j; const int rc = (s0 + rr >= 0) ? rr : -s0;
;           pr[j] = (const unsigned*)(proj + (size_t)((long)t0 + rc) * PP + col); }
;         asm volatile("global_load_dword %0, %10, off\n\tglobal_load_dword %1, %11, off\n\tglobal_load_dword %2, %12, off\n\tglobal_load_dword %3, %13, off\n\tglobal_load_dword %4, %14, off\n\t"
;                      "global_load_dword %5, %15, off\n\tglobal_load_dword %6, %16, off\n\tglobal_load_dword %7, %17, off\n\tglobal_load_dword %8, %18, off\n\tglobal_load_dword %9, %19, off\n\ts_waitcnt vmcnt(0)"
;                      : "=&v"(raw[0]), "=&v"(raw[1]), "=&v"(raw[2]), "=&v"(raw[3]), "=&v"(raw[4]), "=&v"(raw[5]), "=&v"(raw[6]), "=&v"(raw[7]), "=&v"(raw[8]), "=&v"(raw[9])
;                      : "v"(pr[0]), "v"(pr[1]), "v"(pr[2]), "v"(pr[3]), "v"(pr[4]), "v"(pr[5]), "v"(pr[6]), "v"(pr[7]), "v"(pr[8]), "v"(pr[9]) : "memory");
;         asm volatile("global_load_dword %0, %9, off\n\tglobal_load_dword %1, %10, off\n\tglobal_load_dword %2, %11, off\n\tglobal_load_dword %3, %12, off\n\tglobal_load_dword %4, %13, off\n\t"
;                      "global_load_dword %5, %14, off\n\tglobal_load_dword %6, %15, off\n\tglobal_load_dword %7, %16, off\n\tglobal_load_dword %8, %17, off\n\ts_waitcnt vmcnt(0)"
;                      : "=&v"(raw[10]), "=&v"(raw[11]), "=&v"(raw[12]), "=&v"(raw[13]), "=&v"(raw[14]), "=&v"(raw[15]), "=&v"(raw[16]), "=&v"(raw[17]), "=&v"(raw[18])
;                      : "v"(pr[10]), "v"(pr[11]), "v"(pr[12]), "v"(pr[13]), "v"(pr[14]), "v"(pr[15]), "v"(pr[16]), "v"(pr[17]), "v"(pr[18]) : "memory");
.LBB0_1092:
	s_or_b64 exec, exec, s[8:9]
	v_ashrrev_i32_e32 v181, 6, v175
	v_lshlrev_b32_e32 v27, 4, v181
	v_sub_u32_e32 v62, 0, v3
	v_or_b32_e32 v180, 6, v27
	v_add_u32_e32 v84, v27, v3
	v_lshlrev_b32_e32 v3, 4, v175
	v_max_i32_e32 v42, v180, v62
	v_lshrrev_b32_e32 v31, 4, v178
	v_lshlrev_b64 v[4:5], 14, v[34:35]
	v_and_b32_e32 v85, 32, v3
	v_lshrrev_b32_e32 v3, 5, v175
	s_mov_b32 s0, 0x1fffffc
	v_lshlrev_b32_e32 v6, 3, v175
	v_ashrrev_i32_e32 v43, 31, v42
	v_lshl_add_u64 v[66:67], s[66:67], 0, v[4:5]
	v_lshlrev_b32_e32 v4, 1, v178
	v_and_or_b32 v3, v3, s0, v31
	v_and_b32_e32 v6, 64, v6
	v_lshl_add_u64 v[42:43], v[0:1], 0, v[42:43]
	v_lshl_or_b32 v2, v2, 7, v4
	v_add_u32_e32 v5, -3, v27
	v_and_b32_e32 v99, 4, v175
	v_lshl_or_b32 v87, v3, 7, v6
	v_add_u32_e32 v6, -2, v27
	v_add_u32_e32 v8, -1, v27
	v_or_b32_e32 v190, 1, v27
	v_or_b32_e32 v187, 2, v27
	v_or_b32_e32 v185, 3, v27
	v_or_b32_e32 v183, 4, v27
	v_or_b32_e32 v182, 5, v27
	v_mul_lo_u32 v194, v43, s3
	v_or_b32_e32 v43, 7, v27
	v_and_or_b32 v93, v4, 2, v99
	v_lshlrev_b32_e32 v70, 2, v2
	v_lshlrev_b32_e32 v2, 1, v2
	v_mov_b32_e32 v3, v30
	v_max_i32_e32 v4, v5, v62
	v_max_i32_e32 v6, v6, v62
	v_max_i32_e32 v8, v8, v62
	v_max_i32_e32 v18, v27, v62
	v_max_i32_e32 v20, v190, v62
	v_max_i32_e32 v22, v187, v62
	v_max_i32_e32 v24, v185, v62
	v_max_i32_e32 v38, v183, v62
	v_max_i32_e32 v40, v182, v62
	v_max_i32_e32 v44, v43, v62
	v_lshl_add_u64 v[10:11], s[58:59], 0, v[2:3]
	s_mov_b64 s[0:1], 0xc00
	v_ashrrev_i32_e32 v5, 31, v4
	v_ashrrev_i32_e32 v7, 31, v6
	v_ashrrev_i32_e32 v9, 31, v8
	v_ashrrev_i32_e32 v19, 31, v18
	v_ashrrev_i32_e32 v21, 31, v20
	v_ashrrev_i32_e32 v23, 31, v22
	v_ashrrev_i32_e32 v25, 31, v24
	v_ashrrev_i32_e32 v39, 31, v38
	v_ashrrev_i32_e32 v41, 31, v40
	v_ashrrev_i32_e32 v45, 31, v44
	v_lshl_add_u64 v[2:3], v[10:11], 0, s[0:1]
	v_lshl_add_u64 v[12:13], v[0:1], 0, v[4:5]
	v_lshl_add_u64 v[14:15], v[0:1], 0, v[6:7]
	v_lshl_add_u64 v[16:17], v[0:1], 0, v[8:9]
	v_lshl_add_u64 v[18:19], v[0:1], 0, v[18:19]
	v_lshl_add_u64 v[20:21], v[0:1], 0, v[20:21]
	v_lshl_add_u64 v[22:23], v[0:1], 0, v[22:23]
	v_lshl_add_u64 v[24:25], v[0:1], 0, v[24:25]
	v_lshl_add_u64 v[38:39], v[0:1], 0, v[38:39]
	v_lshl_add_u64 v[40:41], v[0:1], 0, v[40:41]
	v_lshl_add_u64 v[44:45], v[0:1], 0, v[44:45]
	v_mov_b32_e32 v71, v30
	v_mad_u64_u32 v[4:5], s[0:1], v12, s3, v[2:3]
	v_mad_u64_u32 v[6:7], s[0:1], v14, s3, v[2:3]
	v_mad_u64_u32 v[8:9], s[0:1], v16, s3, v[2:3]
	v_mad_u64_u32 v[36:37], s[0:1], v18, s3, v[2:3]
	v_mad_u64_u32 v[72:73], s[0:1], v20, s3, v[2:3]
	v_mad_u64_u32 v[82:83], s[0:1], v22, s3, v[2:3]
	v_mad_u64_u32 v[88:89], s[0:1], v24, s3, v[2:3]
	v_mad_u64_u32 v[90:91], s[0:1], v38, s3, v[2:3]
	v_mad_u64_u32 v[94:95], s[0:1], v40, s3, v[2:3]
	v_mad_u64_u32 v[96:97], s[0:1], v42, s3, v[2:3]
	v_mad_u64_u32 v[100:101], s[0:1], v44, s3, v[2:3]
	v_lshl_add_u64 v[68:69], s[70:71], 0, v[70:71]
	s_movk_i32 s0, 0x1000
	v_add_co_u32_e32 v64, vcc, s0, v68
	s_movk_i32 s0, 0x4000
	s_nop 0
	v_addc_co_u32_e32 v65, vcc, 0, v69, vcc
	v_add_co_u32_e32 v56, vcc, s0, v68
	s_waitcnt lgkmcnt(0)
	s_barrier
	v_addc_co_u32_e32 v57, vcc, 0, v69, vcc
	global_load_dwordx2 v[74:75], v70, s[70:71]
	global_load_dwordx2 v[76:77], v[56:57], off offset:-4096
	global_load_dwordx2 v[78:79], v[56:57], off offset:2048
	global_load_dwordx2 v[80:81], v[64:65], off offset:2048
	v_or_b32_e32 v192, 8, v27
	v_or_b32_e32 v191, 9, v27
	v_or_b32_e32 v186, 10, v27
	v_max_i32_e32 v46, v192, v62
	v_max_i32_e32 v48, v191, v62
	v_max_i32_e32 v50, v186, v62
	v_ashrrev_i32_e32 v47, 31, v46
	v_ashrrev_i32_e32 v49, 31, v48
	v_ashrrev_i32_e32 v51, 31, v50
	v_lshl_add_u64 v[46:47], v[0:1], 0, v[46:47]
	v_lshl_add_u64 v[48:49], v[0:1], 0, v[48:49]
	v_lshl_add_u64 v[50:51], v[0:1], 0, v[50:51]
	v_mul_lo_u32 v193, v41, s3
	v_mul_lo_u32 v195, v47, s3
	v_mul_lo_u32 v196, v49, s3
	v_mul_lo_u32 v197, v51, s3
	v_or_b32_e32 v184, 11, v27
	v_or_b32_e32 v51, 12, v27
	v_or_b32_e32 v49, 13, v27
	v_or_b32_e32 v47, 14, v27
	v_or_b32_e32 v41, 15, v27
	v_max_i32_e32 v52, v184, v62
	v_max_i32_e32 v54, v51, v62
	v_max_i32_e32 v58, v49, v62
	v_max_i32_e32 v60, v47, v62
	v_max_i32_e32 v62, v41, v62
	v_mul_lo_u32 v13, v13, s3
	v_ashrrev_i32_e32 v53, 31, v52
	v_ashrrev_i32_e32 v55, 31, v54
	v_ashrrev_i32_e32 v59, 31, v58
	v_ashrrev_i32_e32 v61, 31, v60
	v_ashrrev_i32_e32 v63, 31, v62
	v_add_u32_e32 v5, v13, v5
	v_mul_lo_u32 v15, v15, s3
	v_mul_lo_u32 v17, v17, s3
	v_mul_lo_u32 v19, v19, s3
	v_mul_lo_u32 v21, v21, s3
	v_mul_lo_u32 v23, v23, s3
	v_mul_lo_u32 v25, v25, s3
	v_mul_lo_u32 v39, v39, s3
	v_lshl_add_u64 v[52:53], v[0:1], 0, v[52:53]
	v_lshl_add_u64 v[54:55], v[0:1], 0, v[54:55]
	v_lshl_add_u64 v[58:59], v[0:1], 0, v[58:59]
	v_lshl_add_u64 v[60:61], v[0:1], 0, v[60:61]
	v_lshl_add_u64 v[62:63], v[0:1], 0, v[62:63]
	v_cmp_gt_i32_e64 s[8:9], 2, v84
	v_add_u32_e32 v7, v15, v7
	v_add_u32_e32 v9, v17, v9
	v_add_u32_e32 v37, v19, v37
	v_add_u32_e32 v73, v21, v73
	v_add_u32_e32 v83, v23, v83
	v_add_u32_e32 v89, v25, v89
	v_add_u32_e32 v91, v39, v91
	v_add_u32_e32 v95, v193, v95
	v_add_u32_e32 v97, v194, v97
	v_mad_u64_u32 v[102:103], s[0:1], v46, s3, v[2:3]
	v_mad_u64_u32 v[106:107], s[0:1], v48, s3, v[2:3]
	v_mad_u64_u32 v[108:109], s[0:1], v50, s3, v[2:3]
	v_mad_u64_u32 v[112:113], s[0:1], v52, s3, v[2:3]
	v_mul_lo_u32 v198, v53, s3
	v_mad_u64_u32 v[114:115], s[0:1], v54, s3, v[2:3]
	v_mul_lo_u32 v199, v55, s3
	v_mad_u64_u32 v[118:119], s[0:1], v58, s3, v[2:3]
	v_mad_u64_u32 v[120:121], s[0:1], v60, s3, v[2:3]
	v_mad_u64_u32 v[0:1], s[0:1], v62, s3, v[2:3]
	global_load_dword v2, v[4:5], off
	global_load_dword v3, v[6:7], off
	global_load_dword v53, v[8:9], off
	global_load_dword v55, v[36:37], off
	global_load_dword v86, v[72:73], off
	global_load_dword v92, v[82:83], off
	global_load_dword v98, v[88:89], off
	global_load_dword v104, v[90:91], off
	global_load_dword v110, v[94:95], off
	global_load_dword v116, v[96:97], off
	global_load_dword v220, v[4:5], off offset:1024
	global_load_dword v220, v[4:5], off offset:2048
	global_load_dword v220, v[6:7], off offset:1024
	global_load_dword v220, v[6:7], off offset:2048
	global_load_dword v220, v[8:9], off offset:1024
	global_load_dword v220, v[8:9], off offset:2048
	global_load_dword v220, v[36:37], off offset:1024
	global_load_dword v220, v[36:37], off offset:2048
	global_load_dword v220, v[72:73], off offset:1024
	global_load_dword v220, v[72:73], off offset:2048
	global_load_dword v220, v[82:83], off offset:1024
	global_load_dword v220, v[82:83], off offset:2048
	global_load_dword v220, v[88:89], off offset:1024
	global_load_dword v220, v[88:89], off offset:2048
	global_load_dword v220, v[90:91], off offset:1024
	global_load_dword v220, v[90:91], off offset:2048
	global_load_dword v220, v[94:95], off offset:1024
	global_load_dword v220, v[94:95], off offset:2048
	global_load_dword v220, v[96:97], off offset:1024
	global_load_dword v220, v[96:97], off offset:2048
	s_waitcnt vmcnt(0)
; DI float bflo(unsigned u) { return __uint_as_float(u << 16); }
; DI float bfhi(unsigned u) { return __uint_as_float(u & 0xffff0000u); }
; DI float sigmoidf_(float x) { return __builtin_amdgcn_rcpf(1.f + __expf(-x)); }
; DI void gdn_prep_unit(const Params& p, int U, char* lds) {
;     ...
;         asm volatile("global_load_dword %0, %9, off\n\tglobal_load_dword %1, %10, off\n\tglobal_load_dword %2, %11, off\n\tglobal_load_dword %3, %12, off\n\tglobal_load_dword %4, %13, off\n\t"
;                      "global_load_dword %5, %14, off\n\tglobal_load_dword %6, %15, off\n\tglobal_load_dword %7, %16, off\n\tglobal_load_dword %8, %17, off\n\ts_waitcnt vmcnt(0)"
;                      : "=&v"(raw[10]), "=&v"(raw[11]), "=&v"(raw[12]), "=&v"(raw[13]), "=&v"(raw[14]), "=&v"(raw[15]), "=&v"(raw[16]), "=&v"(raw[17]), "=&v"(raw[18])
;                      : "v"(pr[10]), "v"(pr[11]), "v"(pr[12]), "v"(pr[13]), "v"(pr[14]), "v"(pr[15]), "v"(pr[16]), "v"(pr[17]), "v"(pr[18]) : "memory");
; #pragma unroll
;         for (int j = 0; j < 3; ++j) if (s0 + i0 - 3 + j < 0) raw[j] = 0u;
;       }
;       float y0[16], y1[16], ssr[16];
; #pragma unroll
;       for (int ii = 0; ii < 16; ++ii) {
;         float a0 = w0[0] * bflo(raw[ii]) + w0[1] * bflo(raw[ii + 1]) + w0[2] * bflo(raw[ii + 2]) + w0[3] * bflo(raw[ii + 3]);
;         float a1 = w1[0] * bfhi(raw[ii]) + w1[1] * bfhi(raw[ii + 1]) + w1[2] * bfhi(raw[ii + 2]) + w1[3] * bfhi(raw[ii + 3]);
;         a0 = a0 * sigmoidf_(a0); a1 = a1 * sigmoidf_(a1);
;         y0[ii] = a0; y1[ii] = a1; ssr[ii] = a0 * a0 + a1 * a1;
	v_cmp_gt_i32_e32 vcc, 3, v84
	v_cndmask_b32_e64 v5, v3, 0, s[8:9]
	v_cmp_gt_i32_e64 s[10:11], 1, v84
	v_cndmask_b32_e64 v4, v2, 0, vcc
	v_lshlrev_b32_e32 v6, 16, v5
	v_and_b32_e32 v7, 0xffff0000, v5
	v_cndmask_b32_e64 v8, v53, 0, s[10:11]
	v_lshlrev_b32_e32 v2, 16, v4
	v_and_b32_e32 v3, 0xffff0000, v4
	s_waitcnt vmcnt(0)
	v_pk_mul_f32 v[4:5], v[80:81], v[6:7]
	v_lshlrev_b32_e32 v94, 16, v8
	v_pk_fma_f32 v[2:3], v[74:75], v[2:3], v[4:5]
	v_and_b32_e32 v95, 0xffff0000, v8
	v_pk_fma_f32 v[2:3], v[76:77], v[94:95], v[2:3]
	v_lshlrev_b32_e32 v124, 16, v55
	v_and_b32_e32 v125, 0xffff0000, v55
	v_pk_fma_f32 v[2:3], v[78:79], v[124:125], v[2:3]
	s_movk_i32 s0, 0x3000
	v_mul_f32_e32 v4, 0xbfb8aa3b, v2
	v_mul_f32_e32 v5, 0xbfb8aa3b, v3
	v_exp_f32_e32 v4, v4
	v_exp_f32_e32 v5, v5
	v_add_co_u32_e64 v72, s[0:1], s0, v68
	v_add_f32_e32 v4, 1.0, v4
	v_add_f32_e32 v5, 1.0, v5
	v_rcp_f32_e32 v4, v4
	v_rcp_f32_e32 v5, v5
	v_mul_lo_u32 v45, v45, s3
	v_mul_lo_u32 v59, v59, s3
	v_mul_lo_u32 v61, v61, s3
	v_mul_lo_u32 v63, v63, s3
	v_addc_co_u32_e64 v73, s[0:1], 0, v69, s[0:1]
	v_pk_mul_f32 v[82:83], v[2:3], v[4:5]
	v_pk_mul_f32 v[88:89], v[80:81], v[94:95]
	v_add_u32_e32 v101, v45, v101
	v_add_u32_e32 v103, v195, v103
	v_add_u32_e32 v107, v196, v107
	v_add_u32_e32 v109, v197, v109
	v_add_u32_e32 v113, v198, v113
	v_add_u32_e32 v115, v199, v115
	v_add_u32_e32 v119, v59, v119
	v_add_u32_e32 v121, v61, v121
	v_add_u32_e32 v1, v63, v1
	global_load_dword v122, v[100:101], off
	global_load_dword v153, v[102:103], off
	global_load_dword v154, v[106:107], off
	global_load_dword v156, v[108:109], off
	global_load_dword v159, v[112:113], off
	global_load_dword v158, v[114:115], off
	global_load_dword v160, v[118:119], off
	global_load_dword v162, v[120:121], off
	global_load_dword v71, v[0:1], off
	global_load_dword v220, v[100:101], off offset:1024
	global_load_dword v220, v[100:101], off offset:2048
	global_load_dword v220, v[102:103], off offset:1024
	global_load_dword v220, v[102:103], off offset:2048
	global_load_dword v220, v[106:107], off offset:1024
	global_load_dword v220, v[106:107], off offset:2048
	global_load_dword v220, v[108:109], off offset:1024
	global_load_dword v220, v[108:109], off offset:2048
	global_load_dword v220, v[112:113], off offset:1024
	global_load_dword v220, v[112:113], off offset:2048
	global_load_dword v220, v[114:115], off offset:1024
	global_load_dword v220, v[114:115], off offset:2048
	global_load_dword v220, v[118:119], off offset:1024
	global_load_dword v220, v[118:119], off offset:2048
	global_load_dword v220, v[120:121], off offset:1024
	global_load_dword v220, v[120:121], off offset:2048
	global_load_dword v220, v[0:1], off offset:1024
	global_load_dword v220, v[0:1], off offset:2048
	s_waitcnt vmcnt(0)
	v_mul_f32_e32 v0, v83, v83
	v_cmp_lt_i32_e64 s[0:1], v164, v166
	v_pk_fma_f32 v[6:7], v[74:75], v[6:7], v[88:89]
	v_pk_fma_f32 v[4:5], v[82:83], v[82:83], v[0:1] op_sel_hi:[1,1,0]
	v_cndmask_b32_e64 v0, v123, v164, s[0:1]
	v_and_b32_e32 v53, 0xffffffc0, v175
	v_pk_fma_f32 v[6:7], v[76:77], v[124:125], v[6:7]
	v_lshlrev_b32_e32 v106, 16, v86
	v_and_b32_e32 v107, 0xffff0000, v86
	v_lshl_add_u32 v36, v178, 2, v146
	v_lshlrev_b32_e32 v55, 2, v0
	v_add_u32_e32 v0, v29, v53
	s_movk_i32 s0, 0x1100
	v_lshl_add_u32 v5, v183, 2, v29
	v_pk_fma_f32 v[6:7], v[78:79], v[106:107], v[6:7]
	ds_read_b128 v[0:3], v0 offset:512
	ds_read_b128 v[126:129], v5 offset:512
	v_mad_u64_u32 v[8:9], s[0:1], v181, s0, v[36:37]
	v_mul_f32_e32 v5, 0xbfb8aa3b, v6
	v_exp_f32_e32 v5, v5
	v_mul_f32_e32 v9, 0xbfb8aa3b, v7
	v_exp_f32_e32 v9, v9
	s_waitcnt lgkmcnt(1)
	v_mul_f32_e32 v84, 0x3db504f3, v0
	v_add_f32_e32 v5, 1.0, v5
	v_rcp_f32_e32 v88, v5
	v_add_f32_e32 v5, 1.0, v9
	v_rcp_f32_e32 v89, v5
	v_and_b32_e32 v0, 16, v27
	v_or3_b32 v0, v85, v0, v87
	v_lshl_or_b32 v90, v0, 3, v93
	v_pk_mul_f32 v[88:89], v[6:7], v[88:89]
	v_mul_f32_e32 v86, 0x3db504f3, v1
	v_mul_f32_e32 v0, v89, v89
	v_pk_fma_f32 v[138:139], v[88:89], v[88:89], v[0:1] op_sel_hi:[1,1,0]
	v_pk_mul_f32 v[0:1], v[80:81], v[124:125]
	v_lshlrev_b32_e32 v6, 16, v92
	v_pk_fma_f32 v[0:1], v[74:75], v[94:95], v[0:1]
	v_and_b32_e32 v7, 0xffff0000, v92
	v_pk_fma_f32 v[0:1], v[76:77], v[106:107], v[0:1]
	v_mad_u64_u32 v[36:37], s[0:1], v190, s18, v[36:37]
	v_pk_fma_f32 v[0:1], v[78:79], v[6:7], v[0:1]
	v_pk_mul_f32 v[100:101], v[80:81], v[106:107]
	v_mul_f32_e32 v9, 0xbfb8aa3b, v0
	v_exp_f32_e32 v9, v9
	v_mul_f32_e32 v37, 0xbfb8aa3b, v1
	v_exp_f32_e32 v37, v37
	v_pk_fma_f32 v[100:101], v[74:75], v[124:125], v[100:101]
	v_add_f32_e32 v9, 1.0, v9
	v_rcp_f32_e32 v94, v9
	v_add_f32_e32 v9, 1.0, v37
	v_rcp_f32_e32 v95, v9
	v_bitop3_b32 v5, v27, 17, 1 bitop3:0xc8
	v_pk_fma_f32 v[100:101], v[76:77], v[6:7], v[100:101]
	v_or3_b32 v5, v85, v5, v87
	v_pk_mul_f32 v[94:95], v[0:1], v[94:95]
	v_lshl_or_b32 v96, v5, 3, v93
	v_mul_f32_e32 v0, v95, v95
	v_pk_fma_f32 v[136:137], v[94:95], v[94:95], v[0:1] op_sel_hi:[1,1,0]
	v_lshlrev_b32_e32 v0, 16, v98
	v_and_b32_e32 v1, 0xffff0000, v98
	v_pk_fma_f32 v[100:101], v[78:79], v[0:1], v[100:101]
	v_mul_f32_e32 v92, 0x3db504f3, v2
	v_mul_f32_e32 v5, 0xbfb8aa3b, v100
	v_exp_f32_e32 v5, v5
	v_mul_f32_e32 v9, 0xbfb8aa3b, v101
	v_exp_f32_e32 v9, v9
	v_bitop3_b32 v2, v27, 18, 2 bitop3:0xc8
	v_add_f32_e32 v5, 1.0, v5
	v_rcp_f32_e32 v108, v5
	v_add_f32_e32 v5, 1.0, v9
	v_rcp_f32_e32 v109, v5
	v_or3_b32 v2, v85, v2, v87
	v_lshl_or_b32 v102, v2, 3, v93
	v_mul_f32_e32 v98, 0x3db504f3, v3
	v_pk_mul_f32 v[100:101], v[100:101], v[108:109]
	v_pk_mul_f32 v[108:109], v[80:81], v[6:7]
	v_mul_f32_e32 v2, v101, v101
	v_pk_fma_f32 v[106:107], v[74:75], v[106:107], v[108:109]
	v_pk_fma_f32 v[134:135], v[100:101], v[100:101], v[2:3] op_sel_hi:[1,1,0]
	v_lshlrev_b32_e32 v2, 16, v104
	v_and_b32_e32 v3, 0xffff0000, v104
	v_pk_fma_f32 v[106:107], v[76:77], v[0:1], v[106:107]
	v_lshlrev_b32_e32 v130, 16, v110
	v_pk_fma_f32 v[106:107], v[78:79], v[2:3], v[106:107]
	v_and_b32_e32 v131, 0xffff0000, v110
	v_mul_f32_e32 v9, 0xbfb8aa3b, v106
	v_exp_f32_e32 v9, v9
	v_mul_f32_e32 v37, 0xbfb8aa3b, v107
	v_exp_f32_e32 v37, v37
	v_lshlrev_b32_e32 v148, 16, v116
	v_add_f32_e32 v9, 1.0, v9
	v_rcp_f32_e32 v112, v9
	v_add_f32_e32 v9, 1.0, v37
	v_rcp_f32_e32 v113, v9
	v_and_b32_e32 v149, 0xffff0000, v116
	v_lshlrev_b32_e32 v150, 16, v122
	v_and_b32_e32 v151, 0xffff0000, v122
	v_pk_mul_f32 v[106:107], v[106:107], v[112:113]
	v_pk_mul_f32 v[112:113], v[80:81], v[0:1]
	v_mul_f32_e32 v104, v107, v107
	v_pk_fma_f32 v[6:7], v[74:75], v[6:7], v[112:113]
	v_pk_fma_f32 v[132:133], v[106:107], v[106:107], v[104:105] op_sel_hi:[1,1,0]
	v_pk_fma_f32 v[6:7], v[76:77], v[2:3], v[6:7]
	s_waitcnt lgkmcnt(0)
; DI float bflo(unsigned u) { return __uint_as_float(u << 16); }
; DI float bfhi(unsigned u) { return __uint_as_float(u & 0xffff0000u); }
; DI float dpp_xor8(float v) { return __uint_as_float((unsigned)__builtin_amdgcn_update_dpp(0, (int)__float_as_uint(v), 0x128, 0xF, 0xF, true)); }
; DI float swap32sum(float a, float b) { const auto r = __builtin_amdgcn_permlane32_swap(__float_as_uint(a), __float_as_uint(b), false, false); return __uint_as_float(r[0]) + __uint_as_float(r[1]); }
; DI float swap16sum(float a, float b) { const auto r = __builtin_amdgcn_permlane16_swap(__float_as_uint(a), __float_as_uint(b), false, false); return __uint_as_float(r[0]) + __uint_as_float(r[1]); }
; DI float sigmoidf_(float x) { return __builtin_amdgcn_rcpf(1.f + __expf(-x)); }
; DI void gdn_prep_unit(const Params& p, int U, char* lds) {
;     ...
;       float y0[16], y1[16], ssr[16];
; #pragma unroll
;       for (int ii = 0; ii < 16; ++ii) {
;         float a0 = w0[0] * bflo(raw[ii]) + w0[1] * bflo(raw[ii + 1]) + w0[2] * bflo(raw[ii + 2]) + w0[3] * bflo(raw[ii + 3]);
;         float a1 = w1[0] * bfhi(raw[ii]) + w1[1] * bfhi(raw[ii + 1]) + w1[2] * bfhi(raw[ii + 2]) + w1[3] * bfhi(raw[ii + 3]);
;         a0 = a0 * sigmoidf_(a0); a1 = a1 * sigmoidf_(a1);
;         y0[ii] = a0; y1[ii] = a1; ssr[ii] = a0 * a0 + a1 * a1;
;       }
;       if (X < 2) {
;         const bool b3 = (lane & 8) != 0, b2 = (lane & 4) != 0;
;         float r8[8], r4[4], r2[2];
; #pragma unroll
;         for (int j = 0; j < 8; ++j) r8[j] = swap32sum(ssr[j], ssr[8 + j]);
; #pragma unroll
;         for (int j = 0; j < 4; ++j) r4[j] = swap16sum(r8[j], r8[4 + j]);
; #pragma unroll
;         for (int j = 0; j < 2; ++j) { const float keep = b3 ? r4[2 + j] : r4[j], send = b3 ? r4[j] : r4[2 + j]; r2[j] = keep + dpp_xor8(send); }
;         float r1 = (b2 ? r2[1] : r2[0]) + __shfl_xor(b2 ? r2[0] : r2[1], 4);
;         r1 += __uint_as_float((unsigned)__builtin_amdgcn_update_dpp(0, (int)__float_as_uint(r1), 0x4E, 0xF, 0xF, true));
;         r1 += __uint_as_float((unsigned)__builtin_amdgcn_update_dpp(0, (int)__float_as_uint(r1), 0xB1, 0xF, 0xF, true));
; #pragma unroll
;         for (int ii = 0; ii < 16; ++ii) ssr[ii] = __uint_as_float((unsigned)__builtin_amdgcn_readlane((int)__float_as_uint(r1), 4 * ii));
	v_mul_f32_e32 v104, 0x3db504f3, v126
	v_pk_fma_f32 v[6:7], v[78:79], v[130:131], v[6:7]
	v_mul_f32_e32 v110, 0x3db504f3, v127
	v_mul_f32_e32 v9, 0xbfb8aa3b, v6
	v_exp_f32_e32 v9, v9
	v_mul_f32_e32 v37, 0xbfb8aa3b, v7
	v_exp_f32_e32 v37, v37
	v_lshlrev_b32_e32 v202, 16, v154
	v_add_f32_e32 v9, 1.0, v9
	v_rcp_f32_e32 v114, v9
	v_add_f32_e32 v9, 1.0, v37
	v_rcp_f32_e32 v115, v9
	v_and_b32_e32 v203, 0xffff0000, v154
	v_pk_mul_f32 v[154:155], v[80:81], v[150:151]
	v_lshlrev_b32_e32 v152, 16, v153
	v_pk_mul_f32 v[114:115], v[6:7], v[114:115]
	v_and_b32_e32 v153, 0xffff0000, v153
	v_mul_f32_e32 v6, v115, v115
	v_pk_fma_f32 v[140:141], v[114:115], v[114:115], v[6:7] op_sel_hi:[1,1,0]
	v_pk_mul_f32 v[6:7], v[80:81], v[2:3]
	v_bitop3_b32 v5, v27, 19, 3 bitop3:0xc8
	v_pk_fma_f32 v[0:1], v[74:75], v[0:1], v[6:7]
	v_or3_b32 v5, v85, v5, v87
	v_pk_fma_f32 v[0:1], v[76:77], v[130:131], v[0:1]
	v_lshl_or_b32 v108, v5, 3, v93
	v_pk_fma_f32 v[0:1], v[78:79], v[148:149], v[0:1]
	v_bitop3_b32 v5, v27, 20, 4 bitop3:0xc8
	v_mul_f32_e32 v6, 0xbfb8aa3b, v0
	v_mul_f32_e32 v7, 0xbfb8aa3b, v1
	v_exp_f32_e32 v6, v6
	v_exp_f32_e32 v7, v7
	v_or3_b32 v5, v85, v5, v87
	v_lshl_or_b32 v112, v5, 3, v93
	v_add_f32_e32 v6, 1.0, v6
	v_add_f32_e32 v7, 1.0, v7
	v_rcp_f32_e32 v6, v6
	v_rcp_f32_e32 v7, v7
	v_bitop3_b32 v5, v27, 21, 5 bitop3:0xc8
	v_or3_b32 v5, v85, v5, v87
	v_lshl_or_b32 v118, v5, 3, v93
	v_pk_mul_f32 v[120:121], v[0:1], v[6:7]
	v_bitop3_b32 v5, v27, 22, 6 bitop3:0xc8
	v_mul_f32_e32 v0, v121, v121
	v_pk_fma_f32 v[142:143], v[120:121], v[120:121], v[0:1] op_sel_hi:[1,1,0]
	v_pk_mul_f32 v[0:1], v[80:81], v[130:131]
	v_or3_b32 v5, v85, v5, v87
	v_pk_fma_f32 v[0:1], v[74:75], v[2:3], v[0:1]
	v_bitop3_b32 v37, v27, 24, 8 bitop3:0xc8
	v_pk_fma_f32 v[0:1], v[76:77], v[148:149], v[0:1]
	v_lshl_or_b32 v6, v5, 3, v93
	v_pk_fma_f32 v[0:1], v[78:79], v[150:151], v[0:1]
	v_or3_b32 v37, v85, v37, v87
	v_mul_f32_e32 v2, 0xbfb8aa3b, v0
	v_mul_f32_e32 v3, 0xbfb8aa3b, v1
	v_exp_f32_e32 v2, v2
	v_exp_f32_e32 v3, v3
	v_ashrrev_i32_e32 v7, 31, v6
	v_lshl_add_u64 v[124:125], v[6:7], 1, v[66:67]
	v_add_f32_e32 v2, 1.0, v2
	v_add_f32_e32 v3, 1.0, v3
	v_rcp_f32_e32 v2, v2
	v_rcp_f32_e32 v3, v3
	v_mul_f32_e32 v116, 0x3db504f3, v128
	v_mul_f32_e32 v122, 0x3db504f3, v129
	v_and_b32_e32 v200, 8, v175
	v_pk_mul_f32 v[126:127], v[0:1], v[2:3]
	v_bitop3_b32 v2, v27, 23, 7 bitop3:0xc8
	v_mul_f32_e32 v0, v127, v127
	v_pk_fma_f32 v[144:145], v[126:127], v[126:127], v[0:1] op_sel_hi:[1,1,0]
	v_pk_mul_f32 v[0:1], v[80:81], v[148:149]
	v_pk_fma_f32 v[148:149], v[74:75], v[148:149], v[154:155]
	v_pk_fma_f32 v[0:1], v[74:75], v[130:131], v[0:1]
	v_pk_fma_f32 v[148:149], v[76:77], v[152:153], v[148:149]
	v_pk_fma_f32 v[0:1], v[76:77], v[150:151], v[0:1]
	v_pk_fma_f32 v[148:149], v[78:79], v[202:203], v[148:149]
	v_pk_fma_f32 v[0:1], v[78:79], v[152:153], v[0:1]
	v_mul_f32_e32 v133, 0xbfb8aa3b, v148
	v_exp_f32_e32 v133, v133
	v_mul_f32_e32 v135, 0xbfb8aa3b, v149
	v_exp_f32_e32 v135, v135
	v_mul_f32_e32 v3, 0xbfb8aa3b, v0
	v_add_f32_e32 v133, 1.0, v133
	v_rcp_f32_e32 v204, v133
	v_add_f32_e32 v133, 1.0, v135
	v_rcp_f32_e32 v205, v133
	v_mul_f32_e32 v5, 0xbfb8aa3b, v1
	v_exp_f32_e32 v3, v3
	v_exp_f32_e32 v5, v5
	v_pk_mul_f32 v[148:149], v[148:149], v[204:205]
	v_lshl_or_b32 v154, v37, 3, v93
	v_mul_f32_e32 v204, v149, v149
	v_pk_fma_f32 v[204:205], v[148:149], v[148:149], v[204:205] op_sel_hi:[1,1,0]
	v_or3_b32 v6, v85, v2, v87
	s_nop 0
	v_permlane32_swap_b32_e32 v138, v204
	v_add_f32_e32 v37, v138, v204
	v_lshlrev_b32_e32 v204, 16, v156
	v_and_b32_e32 v205, 0xffff0000, v156
	v_pk_mul_f32 v[156:157], v[80:81], v[152:153]
	v_add_f32_e32 v2, 1.0, v3
	v_pk_fma_f32 v[150:151], v[74:75], v[150:151], v[156:157]
	v_add_f32_e32 v3, 1.0, v5
	v_pk_fma_f32 v[150:151], v[76:77], v[202:203], v[150:151]
	v_rcp_f32_e32 v2, v2
	v_pk_fma_f32 v[150:151], v[78:79], v[204:205], v[150:151]
	v_rcp_f32_e32 v3, v3
	v_mul_f32_e32 v133, 0xbfb8aa3b, v150
	v_exp_f32_e32 v133, v133
	v_mul_f32_e32 v135, 0xbfb8aa3b, v151
	v_exp_f32_e32 v135, v135
	v_lshl_or_b32 v6, v6, 3, v93
	v_pk_mul_f32 v[130:131], v[0:1], v[2:3]
	v_add_f32_e32 v133, 1.0, v133
	v_ashrrev_i32_e32 v7, 31, v6
	v_mul_f32_e32 v0, v131, v131
	v_rcp_f32_e32 v208, v133
	v_add_f32_e32 v133, 1.0, v135
	v_lshl_add_u64 v[128:129], v[6:7], 1, v[66:67]
	v_pk_fma_f32 v[6:7], v[130:131], v[130:131], v[0:1] op_sel_hi:[1,1,0]
	v_lshl_add_u32 v0, v192, 2, v29
	v_rcp_f32_e32 v209, v133
	ds_read_b128 v[0:3], v0 offset:512
	v_permlane32_swap_b32_e32 v4, v6
	v_pk_mul_f32 v[150:151], v[150:151], v[208:209]
	v_add_f32_e32 v9, v4, v6
	v_lshl_add_u32 v4, v51, 2, v29
	v_mul_f32_e32 v208, v151, v151
	ds_read_b128 v[4:7], v4 offset:512
	s_waitcnt lgkmcnt(1)
; DI float dpp_xor8(float v) { return __uint_as_float((unsigned)__builtin_amdgcn_update_dpp(0, (int)__float_as_uint(v), 0x128, 0xF, 0xF, true)); }
; DI float swap32sum(float a, float b) { const auto r = __builtin_amdgcn_permlane32_swap(__float_as_uint(a), __float_as_uint(b), false, false); return __uint_as_float(r[0]) + __uint_as_float(r[1]); }
; DI float swap16sum(float a, float b) { const auto r = __builtin_amdgcn_permlane16_swap(__float_as_uint(a), __float_as_uint(b), false, false); return __uint_as_float(r[0]) + __uint_as_float(r[1]); }
; DI void gdn_prep_unit(const Params& p, int U, char* lds) {
;     ...
;       if (X < 2) {
;         const bool b3 = (lane & 8) != 0, b2 = (lane & 4) != 0;
;         float r8[8], r4[4], r2[2];
; #pragma unroll
;         for (int j = 0; j < 8; ++j) r8[j] = swap32sum(ssr[j], ssr[8 + j]);
; #pragma unroll
;         for (int j = 0; j < 4; ++j) r4[j] = swap16sum(r8[j], r8[4 + j]);
; #pragma unroll
;         for (int j = 0; j < 2; ++j) { const float keep = b3 ? r4[2 + j] : r4[j], send = b3 ? r4[j] : r4[2 + j]; r2[j] = keep + dpp_xor8(send); }
;         float r1 = (b2 ? r2[1] : r2[0]) + __shfl_xor(b2 ? r2[0] : r2[1], 4);
;         r1 += __uint_as_float((unsigned)__builtin_amdgcn_update_dpp(0, (int)__float_as_uint(r1), 0x4E, 0xF, 0xF, true));
;         r1 += __uint_as_float((unsigned)__builtin_amdgcn_update_dpp(0, (int)__float_as_uint(r1), 0xB1, 0xF, 0xF, true));
; #pragma unroll
;         for (int ii = 0; ii < 16; ++ii) ssr[ii] = __uint_as_float((unsigned)__builtin_amdgcn_readlane((int)__float_as_uint(r1), 4 * ii));
	v_mul_f32_e32 v138, 0x3db504f3, v1
	v_bitop3_b32 v1, v27, 25, 9 bitop3:0xc8
	v_pk_fma_f32 v[208:209], v[150:151], v[150:151], v[208:209] op_sel_hi:[1,1,0]
	v_or3_b32 v1, v85, v1, v87
	s_nop 0
	v_permlane32_swap_b32_e32 v136, v208
	v_lshl_or_b32 v156, v1, 3, v93
	v_add_f32_e32 v1, v136, v208
	v_pk_mul_f32 v[136:137], v[80:81], v[202:203]
	v_lshlrev_b32_e32 v208, 16, v159
	v_pk_fma_f32 v[136:137], v[74:75], v[152:153], v[136:137]
	v_and_b32_e32 v209, 0xffff0000, v159
	v_pk_fma_f32 v[136:137], v[76:77], v[204:205], v[136:137]
	v_bitop3_b32 v133, v27, 26, 10 bitop3:0xc8
	v_pk_fma_f32 v[136:137], v[78:79], v[208:209], v[136:137]
	v_or3_b32 v133, v85, v133, v87
	v_mul_f32_e32 v135, 0xbfb8aa3b, v136
	v_exp_f32_e32 v135, v135
	v_mul_f32_e32 v139, 0xbfb8aa3b, v137
	v_exp_f32_e32 v139, v139
	v_lshl_or_b32 v152, v133, 3, v93
	v_add_f32_e32 v135, 1.0, v135
	v_rcp_f32_e32 v210, v135
	v_add_f32_e32 v135, 1.0, v139
	v_rcp_f32_e32 v211, v135
	v_bitop3_b32 v133, v27, 27, 11 bitop3:0xc8
	v_or3_b32 v133, v85, v133, v87
	v_cmp_eq_u32_e64 s[0:1], 0, v200
	v_pk_mul_f32 v[136:137], v[136:137], v[210:211]
	v_cmp_eq_u32_e64 s[12:13], 0, v99
	v_mul_f32_e32 v210, v137, v137
	v_pk_fma_f32 v[210:211], v[136:137], v[136:137], v[210:211] op_sel_hi:[1,1,0]
	v_ashrrev_i32_e32 v91, 31, v90
	s_nop 0
	v_permlane32_swap_b32_e32 v134, v210
	v_add_f32_e32 v139, v134, v210
	v_pk_mul_f32 v[134:135], v[80:81], v[204:205]
	v_lshlrev_b32_e32 v210, 16, v158
	v_pk_fma_f32 v[134:135], v[74:75], v[202:203], v[134:135]
	v_and_b32_e32 v211, 0xffff0000, v158
	v_pk_fma_f32 v[134:135], v[76:77], v[208:209], v[134:135]
	v_lshl_or_b32 v158, v133, 3, v93
	v_pk_fma_f32 v[134:135], v[78:79], v[210:211], v[134:135]
	v_lshl_add_u64 v[90:91], v[90:91], 1, v[66:67]
	v_mul_f32_e32 v141, 0xbfb8aa3b, v134
	v_exp_f32_e32 v141, v141
	v_mul_f32_e32 v143, 0xbfb8aa3b, v135
	v_exp_f32_e32 v143, v143
	v_ashrrev_i32_e32 v97, 31, v96
	v_add_f32_e32 v141, 1.0, v141
	v_rcp_f32_e32 v202, v141
	v_add_f32_e32 v141, 1.0, v143
	v_rcp_f32_e32 v203, v141
	v_bitop3_b32 v141, v27, 28, 12 bitop3:0xc8
	v_or3_b32 v141, v85, v141, v87
	v_lshl_add_u64 v[96:97], v[96:97], 1, v[66:67]
	v_pk_mul_f32 v[134:135], v[134:135], v[202:203]
	v_ashrrev_i32_e32 v103, 31, v102
	v_mul_f32_e32 v202, v135, v135
	v_pk_fma_f32 v[202:203], v[134:135], v[134:135], v[202:203] op_sel_hi:[1,1,0]
	v_lshl_add_u64 v[102:103], v[102:103], 1, v[66:67]
	s_nop 0
	v_permlane32_swap_b32_e32 v132, v202
	v_add_f32_e32 v132, v132, v202
	s_nop 1
	v_permlane16_swap_b32_e32 v9, v132
	v_add_f32_e32 v9, v9, v132
	v_pk_mul_f32 v[132:133], v[80:81], v[208:209]
	v_lshlrev_b32_e32 v202, 16, v160
	v_pk_fma_f32 v[132:133], v[74:75], v[204:205], v[132:133]
	v_and_b32_e32 v203, 0xffff0000, v160
	v_pk_fma_f32 v[132:133], v[76:77], v[210:211], v[132:133]
	v_lshl_or_b32 v160, v141, 3, v93
	v_pk_fma_f32 v[132:133], v[78:79], v[202:203], v[132:133]
	v_ashrrev_i32_e32 v109, 31, v108
	v_mul_f32_e32 v143, 0xbfb8aa3b, v132
	v_exp_f32_e32 v143, v143
	v_mul_f32_e32 v145, 0xbfb8aa3b, v133
	v_exp_f32_e32 v145, v145
	v_lshl_add_u64 v[108:109], v[108:109], 1, v[66:67]
	v_add_f32_e32 v143, 1.0, v143
	v_rcp_f32_e32 v204, v143
	v_add_f32_e32 v143, 1.0, v145
	v_rcp_f32_e32 v205, v143
	v_bitop3_b32 v143, v27, 29, 13 bitop3:0xc8
	v_or3_b32 v143, v85, v143, v87
	v_ashrrev_i32_e32 v113, 31, v112
	v_pk_mul_f32 v[132:133], v[132:133], v[204:205]
	v_lshl_add_u64 v[112:113], v[112:113], 1, v[66:67]
	v_mul_f32_e32 v204, v133, v133
	v_pk_fma_f32 v[204:205], v[132:133], v[132:133], v[204:205] op_sel_hi:[1,1,0]
	v_ashrrev_i32_e32 v119, 31, v118
	s_nop 0
	v_permlane32_swap_b32_e32 v140, v204
	v_add_f32_e32 v140, v140, v204
	s_nop 1
	v_permlane16_swap_b32_e32 v37, v140
	v_add_f32_e32 v37, v37, v140
	v_pk_mul_f32 v[140:141], v[80:81], v[210:211]
	v_lshlrev_b32_e32 v204, 16, v162
	v_pk_fma_f32 v[140:141], v[74:75], v[208:209], v[140:141]
	v_and_b32_e32 v205, 0xffff0000, v162
	v_pk_fma_f32 v[140:141], v[76:77], v[202:203], v[140:141]
	v_pk_mul_f32 v[80:81], v[80:81], v[202:203]
	v_pk_fma_f32 v[140:141], v[78:79], v[204:205], v[140:141]
	v_pk_fma_f32 v[74:75], v[74:75], v[210:211], v[80:81]
	v_mul_f32_e32 v145, 0xbfb8aa3b, v140
	v_exp_f32_e32 v145, v145
	v_mul_f32_e32 v162, 0xbfb8aa3b, v141
	v_exp_f32_e32 v162, v162
	v_pk_fma_f32 v[74:75], v[76:77], v[204:205], v[74:75]
	v_add_f32_e32 v145, 1.0, v145
	v_rcp_f32_e32 v208, v145
	v_add_f32_e32 v145, 1.0, v162
	v_rcp_f32_e32 v209, v145
	v_lshl_or_b32 v162, v143, 3, v93
	v_and_b32_e32 v143, 0xffff0000, v71
	v_lshl_add_u64 v[118:119], v[118:119], 1, v[66:67]
	v_pk_mul_f32 v[140:141], v[140:141], v[208:209]
	v_mul_f32_e32 v0, 0x3db504f3, v0
	v_mul_f32_e32 v208, v141, v141
	v_pk_fma_f32 v[208:209], v[140:141], v[140:141], v[208:209] op_sel_hi:[1,1,0]
	v_ashrrev_i32_e32 v155, 31, v154
	s_nop 0
	v_permlane32_swap_b32_e32 v142, v208
	v_add_f32_e32 v142, v142, v208
	s_nop 1
	v_permlane16_swap_b32_e32 v1, v142
	v_add_f32_e32 v1, v1, v142
	v_lshlrev_b32_e32 v142, 16, v71
	v_pk_fma_f32 v[74:75], v[78:79], v[142:143], v[74:75]
	v_cndmask_b32_e64 v78, v1, v9, s[0:1]
	v_mul_f32_e32 v71, 0xbfb8aa3b, v74
	v_exp_f32_e32 v71, v71
	v_mul_f32_e32 v76, 0xbfb8aa3b, v75
	v_exp_f32_e32 v77, v76
	v_cndmask_b32_e64 v1, v9, v1, s[0:1]
	v_add_f32_e32 v71, 1.0, v71
	v_rcp_f32_e32 v76, v71
	v_add_f32_e32 v71, 1.0, v77
	v_rcp_f32_e32 v77, v71
	v_add_f32_dpp v1, v1, v78 row_ror:8 row_mask:0xf bank_mask:0xf bound_ctrl:1
	v_bitop3_b32 v9, v27, 30, 14 bitop3:0xc8
	v_or3_b32 v9, v85, v9, v87
	v_pk_mul_f32 v[74:75], v[74:75], v[76:77]
	v_lshl_add_u64 v[154:155], v[154:155], 1, v[66:67]
	v_mul_f32_e32 v76, v75, v75
	v_pk_fma_f32 v[76:77], v[74:75], v[74:75], v[76:77] op_sel_hi:[1,1,0]
	v_ashrrev_i32_e32 v157, 31, v156
	s_nop 0
	v_permlane32_swap_b32_e32 v144, v76
	v_add_f32_e32 v71, v144, v76
	s_nop 1
	v_permlane16_swap_b32_e32 v139, v71
	v_add_f32_e32 v71, v139, v71
	v_cndmask_b32_e64 v76, v71, v37, s[0:1]
	v_cndmask_b32_e64 v37, v37, v71, s[0:1]
	v_lshl_add_u64 v[156:157], v[156:157], 1, v[66:67]
	v_mul_f32_e32 v2, 0x3db504f3, v2
	v_add_f32_dpp v37, v37, v76 row_ror:8 row_mask:0xf bank_mask:0xf bound_ctrl:1
	v_cndmask_b32_e64 v71, v37, v1, s[12:13]
	v_cndmask_b32_e64 v1, v1, v37, s[12:13]
	ds_bpermute_b32 v1, v55, v1
	v_lshl_or_b32 v76, v9, 3, v93
	v_ashrrev_i32_e32 v153, 31, v152
	v_lshl_add_u64 v[152:153], v[152:153], 1, v[66:67]
	v_ashrrev_i32_e32 v159, 31, v158
	s_waitcnt lgkmcnt(0)
; DI unsigned pk2(float lo, float hi) { f32x2 v = {lo, hi}; bf16x2_t b = __builtin_convertvector(v, bf16x2_t); return __builtin_bit_cast(unsigned, b); }
; DI void gdn_prep_unit(const Params& p, int U, char* lds) {
;     ...
;         float r1 = (b2 ? r2[1] : r2[0]) + __shfl_xor(b2 ? r2[0] : r2[1], 4);
;         r1 += __uint_as_float((unsigned)__builtin_amdgcn_update_dpp(0, (int)__float_as_uint(r1), 0x4E, 0xF, 0xF, true));
;         r1 += __uint_as_float((unsigned)__builtin_amdgcn_update_dpp(0, (int)__float_as_uint(r1), 0xB1, 0xF, 0xF, true));
; #pragma unroll
;         for (int ii = 0; ii < 16; ++ii) ssr[ii] = __uint_as_float((unsigned)__builtin_amdgcn_readlane((int)__float_as_uint(r1), 4 * ii));
;       }
; #pragma unroll
;       for (int ii = 0; ii < 16; ++ii) {
;         const int i = i0 + ii;
;         float a0 = y0[ii], a1 = y1[ii];
;         if (X < 2) { const float rn = rsqrtf(ssr[ii] + 1e-6f); a0 *= rn; a1 *= rn; }
;         *(unsigned*)(dst + i * QP + 2 * lane) = pk2(a0, a1);
;         if (X == 0) {
;           const float f = 0.08838834764831845f * gcs[128 + i];
;           const int d = 2 * lane, mm = d >> 5, ss2 = (d >> 4) & 1, aa = (d >> 3) & 1, hh = (d >> 2) & 1, bb = d & 3;
;           const int lp = (i & 31) + 32 * hh;
;           *(unsigned*)(QF + (size_t)(((((i >> 5) * 4 + mm) * 2 + ss2) * 64 + lp) * 8 + 4 * aa + bb)) = pk2(a0 * f, a1 * f);
	v_add_f32_e32 v1, v71, v1
	v_lshl_add_u64 v[158:159], v[158:159], 1, v[66:67]
	v_ashrrev_i32_e32 v161, 31, v160
	v_add_f32_dpp v1, v1, v1 quad_perm:[2,3,0,1] row_mask:0xf bank_mask:0xf bound_ctrl:1
	v_lshl_add_u64 v[160:161], v[160:161], 1, v[66:67]
	v_ashrrev_i32_e32 v163, 31, v162
	v_add_f32_dpp v1, v1, v1 quad_perm:[1,0,3,2] row_mask:0xf bank_mask:0xf bound_ctrl:1
	v_lshl_add_u64 v[162:163], v[162:163], 1, v[66:67]
	v_readlane_b32 s15, v1, 0
	v_readlane_b32 s14, v1, 4
	v_readlane_b32 s75, v1, 8
	v_readlane_b32 s74, v1, 12
	v_pk_add_f32 v[78:79], s[14:15], v[32:33] op_sel_hi:[1,0]
	v_readlane_b32 s79, v1, 16
	v_mul_f32_e32 v9, 0x4b800000, v79
	v_cmp_gt_f32_e64 s[14:15], s19, v79
	v_readlane_b32 s78, v1, 20
	v_readlane_b32 s81, v1, 24
	v_cndmask_b32_e64 v9, v79, v9, s[14:15]
	v_rsq_f32_e32 v9, v9
	v_readlane_b32 s80, v1, 28
	v_readlane_b32 s61, v1, 32
	v_readlane_b32 s60, v1, 36
	v_readlane_b32 s51, v1, 40
	v_readlane_b32 s50, v1, 44
	v_readlane_b32 s49, v1, 48
	v_readlane_b32 s48, v1, 52
	v_readlane_b32 s45, v1, 56
	v_readlane_b32 s44, v1, 60
	v_mul_f32_e32 v1, 0x45800000, v9
	v_cndmask_b32_e64 v80, v9, v1, s[14:15]
	v_pk_mul_f32 v[80:81], v[80:81], v[82:83] op_sel_hi:[0,1]
	v_cvt_pk_bf16_f32 v1, v80, v81
	ds_write_b32 v8, v1
	v_mul_f32_e32 v1, 0x4b800000, v78
	v_cmp_gt_f32_e64 s[14:15], s19, v78
	v_ashrrev_i32_e32 v77, 31, v76
	v_lshl_add_u64 v[76:77], v[76:77], 1, v[66:67]
	v_cndmask_b32_e64 v1, v78, v1, s[14:15]
	v_rsq_f32_e32 v1, v1
	v_pk_mul_f32 v[78:79], v[80:81], v[84:85] op_sel_hi:[1,0]
	v_pk_add_f32 v[80:81], s[74:75], v[32:33] op_sel_hi:[1,0]
	v_cvt_pk_bf16_f32 v9, v78, v79
	global_store_dword v[90:91], v9, off
	v_mul_f32_e32 v9, 0x45800000, v1
	v_cndmask_b32_e64 v78, v1, v9, s[14:15]
	v_mul_f32_e32 v9, 0x4b800000, v81
	v_cmp_gt_f32_e64 s[14:15], s19, v81
	v_pk_mul_f32 v[78:79], v[78:79], v[88:89] op_sel_hi:[0,1]
	v_cvt_pk_bf16_f32 v1, v78, v79
	v_cndmask_b32_e64 v9, v81, v9, s[14:15]
	v_rsq_f32_e32 v9, v9
	v_pk_mul_f32 v[78:79], v[78:79], v[86:87] op_sel_hi:[1,0]
	s_nop 0
	v_cvt_pk_bf16_f32 v37, v78, v79
	global_store_dword v[96:97], v37, off
	v_mul_f32_e32 v37, 0x45800000, v9
	v_cndmask_b32_e64 v78, v9, v37, s[14:15]
	v_pk_mul_f32 v[78:79], v[78:79], v[94:95] op_sel_hi:[0,1]
	v_cvt_pk_bf16_f32 v9, v78, v79
	ds_write2_b32 v36, v1, v9 offset1:68
	v_mul_f32_e32 v1, 0x4b800000, v80
	v_cmp_gt_f32_e64 s[14:15], s19, v80
	v_pk_mul_f32 v[78:79], v[78:79], v[92:93] op_sel_hi:[1,0]
	s_nop 0
	v_cndmask_b32_e64 v1, v80, v1, s[14:15]
	v_rsq_f32_e32 v1, v1
	v_cvt_pk_bf16_f32 v9, v78, v79
	global_store_dword v[102:103], v9, off
	v_pk_add_f32 v[80:81], s[78:79], v[32:33] op_sel_hi:[1,0]
	v_mul_f32_e32 v9, 0x45800000, v1
	v_cndmask_b32_e64 v78, v1, v9, s[14:15]
	v_mul_f32_e32 v9, 0x4b800000, v81
	v_cmp_gt_f32_e64 s[14:15], s19, v81
	v_pk_mul_f32 v[78:79], v[78:79], v[100:101] op_sel_hi:[0,1]
	v_cvt_pk_bf16_f32 v1, v78, v79
	v_cndmask_b32_e64 v9, v81, v9, s[14:15]
	v_rsq_f32_e32 v9, v9
	v_pk_mul_f32 v[78:79], v[78:79], v[98:99] op_sel_hi:[1,0]
	s_nop 0
	v_cvt_pk_bf16_f32 v37, v78, v79
	global_store_dword v[108:109], v37, off
	v_mul_f32_e32 v37, 0x45800000, v9
	v_cndmask_b32_e64 v78, v9, v37, s[14:15]
	v_pk_mul_f32 v[78:79], v[78:79], v[106:107] op_sel_hi:[0,1]
	v_cvt_pk_bf16_f32 v9, v78, v79
	ds_write2_b32 v36, v1, v9 offset0:136 offset1:204
	v_mul_f32_e32 v1, 0x4b800000, v80
	v_cmp_gt_f32_e64 s[14:15], s19, v80
	v_pk_mul_f32 v[78:79], v[78:79], v[104:105] op_sel_hi:[1,0]
	s_nop 0
	v_cndmask_b32_e64 v1, v80, v1, s[14:15]
	v_rsq_f32_e32 v1, v1
	v_cvt_pk_bf16_f32 v9, v78, v79
	global_store_dword v[112:113], v9, off
	v_pk_add_f32 v[80:81], s[80:81], v[32:33] op_sel_hi:[1,0]
	v_mul_f32_e32 v9, 0x45800000, v1
	v_cndmask_b32_e64 v78, v1, v9, s[14:15]
	v_mul_f32_e32 v9, 0x4b800000, v81
	v_cmp_gt_f32_e64 s[14:15], s19, v81
	v_pk_mul_f32 v[78:79], v[78:79], v[114:115] op_sel_hi:[0,1]
	v_cvt_pk_bf16_f32 v1, v78, v79
	v_cndmask_b32_e64 v9, v81, v9, s[14:15]
	v_rsq_f32_e32 v9, v9
	v_pk_mul_f32 v[78:79], v[78:79], v[110:111] op_sel_hi:[1,0]
	s_nop 0
	v_cvt_pk_bf16_f32 v37, v78, v79
	global_store_dword v[118:119], v37, off
	v_mul_f32_e32 v37, 0x45800000, v9
	v_cndmask_b32_e64 v78, v9, v37, s[14:15]
	v_pk_mul_f32 v[78:79], v[78:79], v[120:121] op_sel_hi:[0,1]
	v_cvt_pk_bf16_f32 v9, v78, v79
	v_add_u32_e32 v37, 0x400, v36
	ds_write2_b32 v37, v1, v9 offset0:16 offset1:84
	v_mul_f32_e32 v1, 0x4b800000, v80
	v_cmp_gt_f32_e64 s[14:15], s19, v80
	v_pk_mul_f32 v[78:79], v[78:79], v[116:117] op_sel_hi:[1,0]
	s_nop 0
	v_cndmask_b32_e64 v1, v80, v1, s[14:15]
	v_rsq_f32_e32 v1, v1
	v_cvt_pk_bf16_f32 v9, v78, v79
	global_store_dword v[124:125], v9, off
	v_pk_add_f32 v[80:81], s[60:61], v[32:33] op_sel_hi:[1,0]
	v_mul_f32_e32 v9, 0x45800000, v1
	v_cndmask_b32_e64 v78, v1, v9, s[14:15]
	v_mul_f32_e32 v9, 0x4b800000, v81
	v_cmp_gt_f32_e64 s[14:15], s19, v81
	v_pk_mul_f32 v[78:79], v[78:79], v[126:127] op_sel_hi:[0,1]
	v_cvt_pk_bf16_f32 v1, v78, v79
	v_cndmask_b32_e64 v9, v81, v9, s[14:15]
	v_rsq_f32_e32 v9, v9
	v_pk_mul_f32 v[78:79], v[78:79], v[122:123] op_sel_hi:[1,0]
	s_nop 0
	v_cvt_pk_bf16_f32 v71, v78, v79
	global_store_dword v[128:129], v71, off
	v_mul_f32_e32 v71, 0x45800000, v9
	v_cndmask_b32_e64 v78, v9, v71, s[14:15]
	v_pk_mul_f32 v[78:79], v[78:79], v[130:131] op_sel_hi:[0,1]
	v_cvt_pk_bf16_f32 v9, v78, v79
	ds_write2_b32 v37, v1, v9 offset0:152 offset1:220
	v_mul_f32_e32 v1, 0x4b800000, v80
	v_cmp_gt_f32_e64 s[14:15], s19, v80
	v_add_u32_e32 v71, 0x800, v36
	s_nop 0
	v_cndmask_b32_e64 v1, v80, v1, s[14:15]
	v_rsq_f32_e32 v9, v1
	v_pk_mul_f32 v[0:1], v[78:79], v[0:1] op_sel_hi:[1,0]
	v_pk_add_f32 v[78:79], s[50:51], v[32:33] op_sel_hi:[1,0]
; DI unsigned pk2(float lo, float hi) { f32x2 v = {lo, hi}; bf16x2_t b = __builtin_convertvector(v, bf16x2_t); return __builtin_bit_cast(unsigned, b); }
; DI void gdn_prep_unit(const Params& p, int U, char* lds) {
;     ...
;     for (int X = 0; X < 3; ++X) {
;       const int col = 1536 + 512 * X + h * 128 + 2 * lane, cb = 512 * X + h * 128 + 2 * lane;
;       float w0[4], w1[4];
; #pragma unroll
;       for (int j = 0; j < 4; ++j) { w0[j] = p.conv_w[j * 1536 + cb]; w1[j] = p.conv_w[j * 1536 + cb + 1]; }
;       bf16_t* dst = X == 0 ? q_s : (X == 1 ? k_s : v_s);
;       const int i0 = 16 * wid;
;       unsigned raw[19];
;       {
;         const unsigned* pr[19];
; #pragma unroll
;         for (int j = 0; j < 19; ++j) { const int rr = i0 - 3 + j; const int rc = (s0 + rr >= 0) ? rr : -s0;
;           pr[j] = (const unsigned*)(proj + (size_t)((long)t0 + rc) * PP + col); }
;         asm volatile("global_load_dword %0, %10, off\n\tglobal_load_dword %1, %11, off\n\tglobal_load_dword %2, %12, off\n\tglobal_load_dword %3, %13, off\n\tglobal_load_dword %4, %14, off\n\t"
;                      "global_load_dword %5, %15, off\n\tglobal_load_dword %6, %16, off\n\tglobal_load_dword %7, %17, off\n\tglobal_load_dword %8, %18, off\n\tglobal_load_dword %9, %19, off\n\ts_waitcnt vmcnt(0)"
;                      : "=&v"(raw[0]), "=&v"(raw[1]), "=&v"(raw[2]), "=&v"(raw[3]), "=&v"(raw[4]), "=&v"(raw[5]), "=&v"(raw[6]), "=&v"(raw[7]), "=&v"(raw[8]), "=&v"(raw[9])
;                      : "v"(pr[0]), "v"(pr[1]), "v"(pr[2]), "v"(pr[3]), "v"(pr[4]), "v"(pr[5]), "v"(pr[6]), "v"(pr[7]), "v"(pr[8]), "v"(pr[9]) : "memory");
;     ...
;       for (int ii = 0; ii < 16; ++ii) {
;         const int i = i0 + ii;
;         float a0 = y0[ii], a1 = y1[ii];
;         if (X < 2) { const float rn = rsqrtf(ssr[ii] + 1e-6f); a0 *= rn; a1 *= rn; }
;         *(unsigned*)(dst + i * QP + 2 * lane) = pk2(a0, a1);
;         if (X == 0) {
;           const float f = 0.08838834764831845f * gcs[128 + i];
;           const int d = 2 * lane, mm = d >> 5, ss2 = (d >> 4) & 1, aa = (d >> 3) & 1, hh = (d >> 2) & 1, bb = d & 3;
;           const int lp = (i & 31) + 32 * hh;
;           *(unsigned*)(QF + (size_t)(((((i >> 5) * 4 + mm) * 2 + ss2) * 64 + lp) * 8 + 4 * aa + bb)) = pk2(a0 * f, a1 * f);
;         }
	v_cvt_pk_bf16_f32 v0, v0, v1
	global_store_dword v[154:155], v0, off
	v_mul_f32_e32 v0, 0x45800000, v9
	v_cndmask_b32_e64 v0, v9, v0, s[14:15]
	v_mul_f32_e32 v37, 0x4b800000, v79
	v_cmp_gt_f32_e64 s[14:15], s19, v79
	v_pk_mul_f32 v[0:1], v[0:1], v[148:149] op_sel_hi:[0,1]
	v_cvt_pk_bf16_f32 v9, v0, v1
	v_cndmask_b32_e64 v37, v79, v37, s[14:15]
	v_rsq_f32_e32 v37, v37
	v_pk_mul_f32 v[0:1], v[0:1], v[138:139] op_sel_hi:[1,0]
	s_nop 0
	v_cvt_pk_bf16_f32 v0, v0, v1
	global_store_dword v[156:157], v0, off
	v_mul_f32_e32 v0, 0x45800000, v37
	v_cndmask_b32_e64 v0, v37, v0, s[14:15]
	v_pk_mul_f32 v[0:1], v[150:151], v[0:1] op_sel_hi:[1,0]
	v_cmp_gt_f32_e64 s[14:15], s19, v78
	v_cvt_pk_bf16_f32 v37, v0, v1
	ds_write2_b32 v71, v9, v37 offset0:32 offset1:100
	v_mul_f32_e32 v9, 0x4b800000, v78
	v_cndmask_b32_e64 v9, v78, v9, s[14:15]
	v_rsq_f32_e32 v9, v9
	v_pk_mul_f32 v[0:1], v[0:1], v[2:3] op_sel_hi:[1,0]
	v_mul_f32_e32 v2, 0x3db504f3, v3
	v_cvt_pk_bf16_f32 v0, v0, v1
	global_store_dword v[152:153], v0, off
	v_mul_f32_e32 v0, 0x45800000, v9
	v_cndmask_b32_e64 v0, v9, v0, s[14:15]
	v_pk_mul_f32 v[0:1], v[136:137], v[0:1] op_sel_hi:[1,0]
	s_nop 0
	v_cvt_pk_bf16_f32 v9, v0, v1
	v_pk_mul_f32 v[0:1], v[0:1], v[2:3] op_sel_hi:[1,0]
	v_pk_add_f32 v[2:3], s[48:49], v[32:33] op_sel_hi:[1,0]
	v_cvt_pk_bf16_f32 v0, v0, v1
	v_mul_f32_e32 v37, 0x4b800000, v3
	v_cmp_gt_f32_e64 s[14:15], s19, v3
	global_store_dword v[158:159], v0, off
	v_mul_f32_e32 v0, 0x3db504f3, v4
	v_cndmask_b32_e64 v3, v3, v37, s[14:15]
	v_rsq_f32_e32 v3, v3
	s_nop 0
	v_mul_f32_e32 v1, 0x45800000, v3
	v_cndmask_b32_e64 v4, v3, v1, s[14:15]
	v_pk_mul_f32 v[78:79], v[134:135], v[4:5] op_sel_hi:[1,0]
	v_cmp_gt_f32_e64 s[14:15], s19, v2
	v_cvt_pk_bf16_f32 v1, v78, v79
	ds_write2_b32 v71, v9, v1 offset0:168 offset1:236
	v_mul_f32_e32 v1, 0x4b800000, v2
	v_cndmask_b32_e64 v1, v2, v1, s[14:15]
	v_rsq_f32_e32 v2, v1
	v_pk_mul_f32 v[0:1], v[78:79], v[0:1] op_sel_hi:[1,0]
	s_nop 0
	v_cvt_pk_bf16_f32 v0, v0, v1
	global_store_dword v[160:161], v0, off
	v_mul_f32_e32 v0, 0x45800000, v2
	v_cndmask_b32_e64 v0, v2, v0, s[14:15]
	v_pk_mul_f32 v[0:1], v[132:133], v[0:1] op_sel_hi:[1,0]
	v_mul_f32_e32 v2, 0x3db504f3, v5
	v_cvt_pk_bf16_f32 v9, v0, v1
	v_pk_mul_f32 v[0:1], v[0:1], v[2:3] op_sel_hi:[1,0]
	v_pk_add_f32 v[2:3], s[44:45], v[32:33] op_sel_hi:[1,0]
	v_cvt_pk_bf16_f32 v0, v0, v1
	v_mul_f32_e32 v4, 0x4b800000, v3
	v_cmp_gt_f32_e64 s[14:15], s19, v3
	global_store_dword v[162:163], v0, off
	v_mul_f32_e32 v0, 0x3db504f3, v6
	v_cndmask_b32_e64 v3, v3, v4, s[14:15]
	v_rsq_f32_e32 v3, v3
	s_nop 0
	v_mul_f32_e32 v1, 0x45800000, v3
	v_cndmask_b32_e64 v4, v3, v1, s[14:15]
	v_pk_mul_f32 v[4:5], v[140:141], v[4:5] op_sel_hi:[1,0]
	v_add_u32_e32 v3, 0xc00, v36
	v_cvt_pk_bf16_f32 v1, v4, v5
	ds_write2_b32 v3, v9, v1 offset0:48 offset1:116
	v_mul_f32_e32 v1, 0x4b800000, v2
	v_cmp_gt_f32_e64 s[14:15], s19, v2
	v_bitop3_b32 v9, v27, 31, 15 bitop3:0xc8
	v_or3_b32 v9, v85, v9, v87
	v_cndmask_b32_e64 v1, v2, v1, s[14:15]
	v_rsq_f32_e32 v2, v1
	v_pk_mul_f32 v[0:1], v[4:5], v[0:1] op_sel_hi:[1,0]
	s_nop 0
	v_cvt_pk_bf16_f32 v0, v0, v1
	global_store_dword v[76:77], v0, off
	v_mul_f32_e32 v0, 0x45800000, v2
	v_cndmask_b32_e64 v0, v2, v0, s[14:15]
	s_movk_i32 s14, 0x2000
	v_add_co_u32_e64 v2, s[14:15], s14, v68
	v_pk_mul_f32 v[74:75], v[74:75], v[0:1] op_sel_hi:[1,0]
	s_nop 0
	v_addc_co_u32_e64 v3, s[14:15], 0, v69, s[14:15]
	v_cvt_pk_bf16_f32 v0, v74, v75
	s_movk_i32 s14, 0x5000
	ds_write_b32 v36, v0 offset:3808
	v_add_co_u32_e64 v0, s[14:15], s14, v68
	v_mul_f32_e32 v76, 0x3db504f3, v7
	global_load_dwordx2 v[6:7], v[2:3], off
	global_load_dwordx2 v[4:5], v70, s[70:71] offset:2048
	s_nop 0
	global_load_dwordx2 v[70:71], v[72:73], off offset:2048
	v_addc_co_u32_e64 v1, s[14:15], 0, v69, s[14:15]
	global_load_dwordx2 v[68:69], v[0:1], off
	v_pk_mul_f32 v[72:73], v[74:75], v[76:77] op_sel_hi:[1,0]
	s_mov_b64 s[14:15], 0x1000
	v_cvt_pk_bf16_f32 v37, v72, v73
	v_lshl_or_b32 v72, v9, 3, v93
	v_ashrrev_i32_e32 v73, 31, v72
	v_lshl_add_u64 v[66:67], v[72:73], 1, v[66:67]
	global_store_dword v[66:67], v37, off
	v_lshl_add_u64 v[66:67], v[10:11], 0, s[14:15]
	v_mad_u64_u32 v[72:73], s[14:15], v12, s3, v[66:67]
	v_mad_u64_u32 v[74:75], s[14:15], v14, s3, v[66:67]
	v_mad_u64_u32 v[76:77], s[14:15], v16, s3, v[66:67]
	v_mad_u64_u32 v[78:79], s[14:15], v18, s3, v[66:67]
	v_mad_u64_u32 v[80:81], s[14:15], v20, s3, v[66:67]
	v_mad_u64_u32 v[82:83], s[14:15], v22, s3, v[66:67]
	v_mad_u64_u32 v[84:85], s[14:15], v24, s3, v[66:67]
	v_mad_u64_u32 v[86:87], s[14:15], v38, s3, v[66:67]
	v_mad_u64_u32 v[88:89], s[14:15], v40, s3, v[66:67]
	v_mad_u64_u32 v[90:91], s[14:15], v42, s3, v[66:67]
	v_add_u32_e32 v73, v13, v73
	v_add_u32_e32 v75, v15, v75
	v_add_u32_e32 v77, v17, v77
	v_add_u32_e32 v79, v19, v79
	v_add_u32_e32 v81, v21, v81
	v_add_u32_e32 v83, v23, v83
	v_add_u32_e32 v85, v25, v85
	v_add_u32_e32 v87, v39, v87
	v_add_u32_e32 v89, v193, v89
	v_add_u32_e32 v91, v194, v91
	global_load_dword v9, v[72:73], off
	global_load_dword v37, v[74:75], off
	global_load_dword v104, v[76:77], off
	global_load_dword v110, v[78:79], off
	global_load_dword v112, v[80:81], off
	global_load_dword v113, v[82:83], off
	global_load_dword v114, v[84:85], off
	global_load_dword v115, v[86:87], off
	global_load_dword v116, v[88:89], off
	global_load_dword v118, v[90:91], off
	s_waitcnt vmcnt(0)
; DI float bflo(unsigned u) { return __uint_as_float(u << 16); }
; DI float bfhi(unsigned u) { return __uint_as_float(u & 0xffff0000u); }
; DI float sigmoidf_(float x) { return __builtin_amdgcn_rcpf(1.f + __expf(-x)); }
; DI void gdn_prep_unit(const Params& p, int U, char* lds) {
;     ...
;         asm volatile("global_load_dword %0, %9, off\n\tglobal_load_dword %1, %10, off\n\tglobal_load_dword %2, %11, off\n\tglobal_load_dword %3, %12, off\n\tglobal_load_dword %4, %13, off\n\t"
;                      "global_load_dword %5, %14, off\n\tglobal_load_dword %6, %15, off\n\tglobal_load_dword %7, %16, off\n\tglobal_load_dword %8, %17, off\n\ts_waitcnt vmcnt(0)"
;                      : "=&v"(raw[10]), "=&v"(raw[11]), "=&v"(raw[12]), "=&v"(raw[13]), "=&v"(raw[14]), "=&v"(raw[15]), "=&v"(raw[16]), "=&v"(raw[17]), "=&v"(raw[18])
;                      : "v"(pr[10]), "v"(pr[11]), "v"(pr[12]), "v"(pr[13]), "v"(pr[14]), "v"(pr[15]), "v"(pr[16]), "v"(pr[17]), "v"(pr[18]) : "memory");
; #pragma unroll
;         for (int j = 0; j < 3; ++j) if (s0 + i0 - 3 + j < 0) raw[j] = 0u;
;       }
;       float y0[16], y1[16], ssr[16];
; #pragma unroll
;       for (int ii = 0; ii < 16; ++ii) {
;         float a0 = w0[0] * bflo(raw[ii]) + w0[1] * bflo(raw[ii + 1]) + w0[2] * bflo(raw[ii + 2]) + w0[3] * bflo(raw[ii + 3]);
;         float a1 = w1[0] * bfhi(raw[ii]) + w1[1] * bfhi(raw[ii + 1]) + w1[2] * bfhi(raw[ii + 2]) + w1[3] * bfhi(raw[ii + 3]);
;         a0 = a0 * sigmoidf_(a0); a1 = a1 * sigmoidf_(a1);
;         y0[ii] = a0; y1[ii] = a1; ssr[ii] = a0 * a0 + a1 * a1;
	v_mad_u64_u32 v[92:93], s[14:15], v44, s3, v[66:67]
	v_cndmask_b32_e64 v37, v37, 0, s[8:9]
	v_cndmask_b32_e64 v9, v9, 0, vcc
	v_lshlrev_b32_e32 v74, 16, v37
	v_and_b32_e32 v75, 0xffff0000, v37
	v_cndmask_b32_e64 v78, v104, 0, s[10:11]
	v_lshlrev_b32_e32 v72, 16, v9
	v_and_b32_e32 v73, 0xffff0000, v9
	v_and_b32_e32 v79, 0xffff0000, v110
	v_mad_u64_u32 v[94:95], s[14:15], v46, s3, v[66:67]
	v_mad_u64_u32 v[96:97], s[14:15], v48, s3, v[66:67]
	v_mad_u64_u32 v[98:99], s[14:15], v50, s3, v[66:67]
	v_mad_u64_u32 v[100:101], s[14:15], v52, s3, v[66:67]
	v_mad_u64_u32 v[102:103], s[14:15], v54, s3, v[66:67]
	v_mad_u64_u32 v[106:107], s[14:15], v58, s3, v[66:67]
	v_mad_u64_u32 v[108:109], s[14:15], v60, s3, v[66:67]
	v_mad_u64_u32 v[66:67], s[14:15], v62, s3, v[66:67]
	v_add_u32_e32 v67, v63, v67
	v_add_u32_e32 v93, v45, v93
	v_add_u32_e32 v95, v195, v95
	v_add_u32_e32 v97, v196, v97
	v_add_u32_e32 v99, v197, v99
	v_add_u32_e32 v101, v198, v101
	v_add_u32_e32 v103, v199, v103
	v_add_u32_e32 v107, v59, v107
	v_add_u32_e32 v109, v61, v109
	s_waitcnt vmcnt(4)
	v_pk_mul_f32 v[76:77], v[6:7], v[74:75]
	s_waitcnt vmcnt(3)
	v_pk_fma_f32 v[72:73], v[4:5], v[72:73], v[76:77]
	v_lshlrev_b32_e32 v76, 16, v78
	v_and_b32_e32 v77, 0xffff0000, v78
	s_waitcnt vmcnt(2)
	v_pk_fma_f32 v[72:73], v[70:71], v[76:77], v[72:73]
	v_lshlrev_b32_e32 v78, 16, v110
	s_waitcnt vmcnt(1)
	v_pk_fma_f32 v[72:73], v[68:69], v[78:79], v[72:73]
	s_nop 0
	v_mul_f32_e32 v9, 0xbfb8aa3b, v72
	v_exp_f32_e32 v9, v9
	v_mul_f32_e32 v37, 0xbfb8aa3b, v73
	v_exp_f32_e32 v37, v37
	v_add_f32_e32 v9, 1.0, v9
	v_rcp_f32_e32 v80, v9
	v_add_f32_e32 v9, 1.0, v37
	v_rcp_f32_e32 v81, v9
	global_load_dword v9, v[92:93], off
	global_load_dword v37, v[94:95], off
	global_load_dword v104, v[96:97], off
	global_load_dword v110, v[98:99], off
	global_load_dword v122, v[100:101], off
	global_load_dword v124, v[102:103], off
	global_load_dword v125, v[106:107], off
	global_load_dword v126, v[108:109], off
	global_load_dword v127, v[66:67], off
	s_waitcnt vmcnt(0)
	v_lshlrev_b32_e32 v100, 16, v118
	v_and_b32_e32 v101, 0xffff0000, v118
	v_pk_mul_f32 v[66:67], v[72:73], v[80:81]
	v_pk_mul_f32 v[80:81], v[6:7], v[76:77]
	v_mul_f32_e32 v72, v67, v67
	v_pk_fma_f32 v[74:75], v[4:5], v[74:75], v[80:81]
	v_lshlrev_b32_e32 v80, 16, v112
	v_pk_fma_f32 v[74:75], v[70:71], v[78:79], v[74:75]
	v_and_b32_e32 v81, 0xffff0000, v112
	v_pk_fma_f32 v[74:75], v[68:69], v[80:81], v[74:75]
	v_pk_mul_f32 v[86:87], v[6:7], v[80:81]
	v_mul_f32_e32 v73, 0xbfb8aa3b, v74
	v_mul_f32_e32 v82, 0xbfb8aa3b, v75
	v_exp_f32_e32 v73, v73
	v_exp_f32_e32 v82, v82
	v_lshlrev_b32_e32 v112, 16, v37
	v_pk_fma_f32 v[88:89], v[66:67], v[66:67], v[72:73] op_sel_hi:[1,1,0]
	v_add_f32_e32 v72, 1.0, v73
	v_add_f32_e32 v73, 1.0, v82
	v_pk_mul_f32 v[82:83], v[6:7], v[78:79]
	v_rcp_f32_e32 v72, v72
	v_pk_fma_f32 v[76:77], v[4:5], v[76:77], v[82:83]
	v_lshlrev_b32_e32 v82, 16, v113
	v_and_b32_e32 v83, 0xffff0000, v113
	v_pk_fma_f32 v[76:77], v[70:71], v[80:81], v[76:77]
	v_rcp_f32_e32 v73, v73
	v_pk_fma_f32 v[76:77], v[68:69], v[82:83], v[76:77]
	v_pk_fma_f32 v[78:79], v[4:5], v[78:79], v[86:87]
	v_mul_f32_e32 v84, 0xbfb8aa3b, v76
	v_mul_f32_e32 v85, 0xbfb8aa3b, v77
	v_exp_f32_e32 v84, v84
	v_exp_f32_e32 v85, v85
	v_pk_mul_f32 v[72:73], v[74:75], v[72:73]
	v_pk_fma_f32 v[78:79], v[70:71], v[82:83], v[78:79]
	v_add_f32_e32 v84, 1.0, v84
	v_add_f32_e32 v85, 1.0, v85
	v_rcp_f32_e32 v84, v84
	v_rcp_f32_e32 v85, v85
	v_mul_f32_e32 v74, v73, v73
	v_pk_fma_f32 v[90:91], v[72:73], v[72:73], v[74:75] op_sel_hi:[1,1,0]
	v_pk_mul_f32 v[94:95], v[6:7], v[82:83]
	v_pk_mul_f32 v[74:75], v[76:77], v[84:85]
	v_lshlrev_b32_e32 v84, 16, v114
	v_and_b32_e32 v85, 0xffff0000, v114
	v_pk_fma_f32 v[78:79], v[68:69], v[84:85], v[78:79]
	v_mul_f32_e32 v76, v75, v75
	v_mul_f32_e32 v77, 0xbfb8aa3b, v78
	v_mul_f32_e32 v86, 0xbfb8aa3b, v79
	v_exp_f32_e32 v77, v77
	v_exp_f32_e32 v86, v86
	v_pk_fma_f32 v[80:81], v[4:5], v[80:81], v[94:95]
	v_and_b32_e32 v87, 0xffff0000, v115
	v_pk_fma_f32 v[92:93], v[74:75], v[74:75], v[76:77] op_sel_hi:[1,1,0]
	v_add_f32_e32 v76, 1.0, v77
	v_add_f32_e32 v77, 1.0, v86
	v_lshlrev_b32_e32 v86, 16, v115
	v_pk_fma_f32 v[80:81], v[70:71], v[84:85], v[80:81]
	v_rcp_f32_e32 v76, v76
	v_pk_fma_f32 v[80:81], v[68:69], v[86:87], v[80:81]
	v_rcp_f32_e32 v77, v77
	v_mul_f32_e32 v89, 0xbfb8aa3b, v80
	v_exp_f32_e32 v89, v89
	v_mul_f32_e32 v91, 0xbfb8aa3b, v81
	v_exp_f32_e32 v91, v91
	v_pk_mul_f32 v[78:79], v[78:79], v[76:77]
	v_add_f32_e32 v89, 1.0, v89
	v_rcp_f32_e32 v94, v89
	v_add_f32_e32 v89, 1.0, v91
	v_rcp_f32_e32 v95, v89
	v_pk_mul_f32 v[98:99], v[6:7], v[84:85]
	v_mul_f32_e32 v76, v79, v79
	v_pk_fma_f32 v[82:83], v[4:5], v[82:83], v[98:99]
	v_pk_fma_f32 v[96:97], v[78:79], v[78:79], v[76:77] op_sel_hi:[1,1,0]
	v_pk_mul_f32 v[76:77], v[80:81], v[94:95]
	v_lshlrev_b32_e32 v94, 16, v116
	v_and_b32_e32 v95, 0xffff0000, v116
	v_pk_fma_f32 v[82:83], v[70:71], v[86:87], v[82:83]
	v_pk_mul_f32 v[102:103], v[6:7], v[86:87]
	v_pk_fma_f32 v[82:83], v[68:69], v[94:95], v[82:83]
	v_pk_fma_f32 v[84:85], v[4:5], v[84:85], v[102:103]
	v_mul_f32_e32 v81, 0xbfb8aa3b, v82
	v_mul_f32_e32 v89, 0xbfb8aa3b, v83
	v_exp_f32_e32 v81, v81
	v_exp_f32_e32 v89, v89
	v_pk_fma_f32 v[84:85], v[70:71], v[94:95], v[84:85]
	v_mul_f32_e32 v80, v77, v77
	v_pk_fma_f32 v[84:85], v[68:69], v[100:101], v[84:85]
	v_pk_fma_f32 v[98:99], v[76:77], v[76:77], v[80:81] op_sel_hi:[1,1,0]
	v_add_f32_e32 v80, 1.0, v81
	v_add_f32_e32 v81, 1.0, v89
	v_mul_f32_e32 v89, 0xbfb8aa3b, v84
	v_exp_f32_e32 v89, v89
	v_mul_f32_e32 v91, 0xbfb8aa3b, v85
	v_exp_f32_e32 v91, v91
	v_rcp_f32_e32 v80, v80
	v_rcp_f32_e32 v81, v81
; DI float bflo(unsigned u) { return __uint_as_float(u << 16); }
; DI float bfhi(unsigned u) { return __uint_as_float(u & 0xffff0000u); }
; DI float dpp_xor8(float v) { return __uint_as_float((unsigned)__builtin_amdgcn_update_dpp(0, (int)__float_as_uint(v), 0x128, 0xF, 0xF, true)); }
; DI float swap32sum(float a, float b) { const auto r = __builtin_amdgcn_permlane32_swap(__float_as_uint(a), __float_as_uint(b), false, false); return __uint_as_float(r[0]) + __uint_as_float(r[1]); }
; DI float swap16sum(float a, float b) { const auto r = __builtin_amdgcn_permlane16_swap(__float_as_uint(a), __float_as_uint(b), false, false); return __uint_as_float(r[0]) + __uint_as_float(r[1]); }
; DI float sigmoidf_(float x) { return __builtin_amdgcn_rcpf(1.f + __expf(-x)); }
; DI void gdn_prep_unit(const Params& p, int U, char* lds) {
;     ...
;       for (int ii = 0; ii < 16; ++ii) {
;         float a0 = w0[0] * bflo(raw[ii]) + w0[1] * bflo(raw[ii + 1]) + w0[2] * bflo(raw[ii + 2]) + w0[3] * bflo(raw[ii + 3]);
;         float a1 = w1[0] * bfhi(raw[ii]) + w1[1] * bfhi(raw[ii + 1]) + w1[2] * bfhi(raw[ii + 2]) + w1[3] * bfhi(raw[ii + 3]);
;         a0 = a0 * sigmoidf_(a0); a1 = a1 * sigmoidf_(a1);
;         y0[ii] = a0; y1[ii] = a1; ssr[ii] = a0 * a0 + a1 * a1;
;       }
;       if (X < 2) {
;         const bool b3 = (lane & 8) != 0, b2 = (lane & 4) != 0;
;         float r8[8], r4[4], r2[2];
; #pragma unroll
;         for (int j = 0; j < 8; ++j) r8[j] = swap32sum(ssr[j], ssr[8 + j]);
; #pragma unroll
;         for (int j = 0; j < 4; ++j) r4[j] = swap16sum(r8[j], r8[4 + j]);
; #pragma unroll
;         for (int j = 0; j < 2; ++j) { const float keep = b3 ? r4[2 + j] : r4[j], send = b3 ? r4[j] : r4[2 + j]; r2[j] = keep + dpp_xor8(send); }
;         float r1 = (b2 ? r2[1] : r2[0]) + __shfl_xor(b2 ? r2[0] : r2[1], 4);
;         r1 += __uint_as_float((unsigned)__builtin_amdgcn_update_dpp(0, (int)__float_as_uint(r1), 0x4E, 0xF, 0xF, true));
;         r1 += __uint_as_float((unsigned)__builtin_amdgcn_update_dpp(0, (int)__float_as_uint(r1), 0xB1, 0xF, 0xF, true));
; #pragma unroll
;         for (int ii = 0; ii < 16; ++ii) ssr[ii] = __uint_as_float((unsigned)__builtin_amdgcn_readlane((int)__float_as_uint(r1), 4 * ii));
	v_add_f32_e32 v89, 1.0, v89
	v_rcp_f32_e32 v102, v89
	v_add_f32_e32 v89, 1.0, v91
	v_rcp_f32_e32 v103, v89
	v_pk_mul_f32 v[80:81], v[82:83], v[80:81]
	v_pk_mul_f32 v[108:109], v[6:7], v[94:95]
	v_mul_f32_e32 v82, v81, v81
	v_pk_fma_f32 v[86:87], v[4:5], v[86:87], v[108:109]
	v_pk_fma_f32 v[106:107], v[80:81], v[80:81], v[82:83] op_sel_hi:[1,1,0]
	v_pk_mul_f32 v[82:83], v[84:85], v[102:103]
	v_lshlrev_b32_e32 v102, 16, v9
	v_and_b32_e32 v103, 0xffff0000, v9
	v_pk_fma_f32 v[86:87], v[70:71], v[100:101], v[86:87]
	v_pk_mul_f32 v[114:115], v[6:7], v[100:101]
	v_pk_fma_f32 v[86:87], v[68:69], v[102:103], v[86:87]
	v_pk_fma_f32 v[94:95], v[4:5], v[94:95], v[114:115]
	v_mul_f32_e32 v9, 0xbfb8aa3b, v86
	v_exp_f32_e32 v9, v9
	v_mul_f32_e32 v85, 0xbfb8aa3b, v87
	v_exp_f32_e32 v85, v85
	v_and_b32_e32 v113, 0xffff0000, v37
	v_pk_fma_f32 v[94:95], v[70:71], v[102:103], v[94:95]
	v_mul_f32_e32 v84, v83, v83
	v_pk_fma_f32 v[94:95], v[68:69], v[112:113], v[94:95]
	v_add_f32_e32 v9, 1.0, v9
	v_mul_f32_e32 v37, 0xbfb8aa3b, v94
	v_pk_fma_f32 v[108:109], v[82:83], v[82:83], v[84:85] op_sel_hi:[1,1,0]
	v_rcp_f32_e32 v84, v9
	v_add_f32_e32 v9, 1.0, v85
	v_exp_f32_e32 v37, v37
	v_mul_f32_e32 v85, 0xbfb8aa3b, v95
	v_exp_f32_e32 v89, v85
	v_rcp_f32_e32 v85, v9
	v_add_f32_e32 v9, 1.0, v37
	v_rcp_f32_e32 v114, v9
	v_add_f32_e32 v9, 1.0, v89
	v_rcp_f32_e32 v115, v9
	v_pk_mul_f32 v[86:87], v[86:87], v[84:85]
	v_pk_mul_f32 v[120:121], v[6:7], v[102:103]
	v_mul_f32_e32 v84, v87, v87
	v_pk_fma_f32 v[100:101], v[4:5], v[100:101], v[120:121]
	v_pk_fma_f32 v[118:119], v[86:87], v[86:87], v[84:85] op_sel_hi:[1,1,0]
	v_pk_mul_f32 v[84:85], v[94:95], v[114:115]
	v_lshlrev_b32_e32 v114, 16, v104
	v_and_b32_e32 v115, 0xffff0000, v104
	v_pk_fma_f32 v[100:101], v[70:71], v[112:113], v[100:101]
	v_mul_f32_e32 v94, v85, v85
	v_pk_fma_f32 v[100:101], v[68:69], v[114:115], v[100:101]
	v_pk_fma_f32 v[94:95], v[84:85], v[84:85], v[94:95] op_sel_hi:[1,1,0]
	v_mul_f32_e32 v9, 0xbfb8aa3b, v100
	v_exp_f32_e32 v9, v9
	v_mul_f32_e32 v37, 0xbfb8aa3b, v101
	v_exp_f32_e32 v37, v37
	v_permlane32_swap_b32_e32 v88, v94
	v_add_f32_e32 v9, 1.0, v9
	v_rcp_f32_e32 v120, v9
	v_add_f32_e32 v9, 1.0, v37
	v_rcp_f32_e32 v121, v9
	v_add_f32_e32 v9, v88, v94
	v_pk_mul_f32 v[88:89], v[100:101], v[120:121]
	v_pk_mul_f32 v[120:121], v[6:7], v[112:113]
	v_lshlrev_b32_e32 v100, 16, v110
	v_pk_fma_f32 v[102:103], v[4:5], v[102:103], v[120:121]
	v_and_b32_e32 v101, 0xffff0000, v110
	v_pk_fma_f32 v[102:103], v[70:71], v[114:115], v[102:103]
	v_mul_f32_e32 v94, v89, v89
	v_pk_fma_f32 v[102:103], v[68:69], v[100:101], v[102:103]
	v_pk_fma_f32 v[94:95], v[88:89], v[88:89], v[94:95] op_sel_hi:[1,1,0]
	v_mul_f32_e32 v37, 0xbfb8aa3b, v102
	v_exp_f32_e32 v37, v37
	v_mul_f32_e32 v91, 0xbfb8aa3b, v103
	v_exp_f32_e32 v91, v91
	v_permlane32_swap_b32_e32 v90, v94
	v_add_f32_e32 v37, 1.0, v37
	v_rcp_f32_e32 v120, v37
	v_add_f32_e32 v37, 1.0, v91
	v_rcp_f32_e32 v121, v37
	v_add_f32_e32 v37, v90, v94
	v_pk_mul_f32 v[90:91], v[102:103], v[120:121]
	v_pk_mul_f32 v[120:121], v[6:7], v[114:115]
	v_lshlrev_b32_e32 v102, 16, v122
	v_pk_fma_f32 v[112:113], v[4:5], v[112:113], v[120:121]
	v_and_b32_e32 v103, 0xffff0000, v122
	v_pk_fma_f32 v[112:113], v[70:71], v[100:101], v[112:113]
	v_mul_f32_e32 v94, v91, v91
	v_pk_fma_f32 v[112:113], v[68:69], v[102:103], v[112:113]
	s_nop 0
	v_mul_f32_e32 v93, 0xbfb8aa3b, v112
	v_exp_f32_e32 v93, v93
	v_mul_f32_e32 v95, 0xbfb8aa3b, v113
	v_exp_f32_e32 v97, v95
	v_pk_fma_f32 v[94:95], v[90:91], v[90:91], v[94:95] op_sel_hi:[1,1,0]
	v_add_f32_e32 v93, 1.0, v93
	v_rcp_f32_e32 v120, v93
	v_add_f32_e32 v93, 1.0, v97
	v_rcp_f32_e32 v121, v93
	v_permlane32_swap_b32_e32 v92, v94
	v_add_f32_e32 v104, v92, v94
	v_pk_mul_f32 v[92:93], v[112:113], v[120:121]
	v_pk_mul_f32 v[120:121], v[6:7], v[100:101]
	v_lshlrev_b32_e32 v112, 16, v124
	v_pk_fma_f32 v[114:115], v[4:5], v[114:115], v[120:121]
	v_and_b32_e32 v113, 0xffff0000, v124
	v_pk_fma_f32 v[114:115], v[70:71], v[102:103], v[114:115]
	v_mul_f32_e32 v94, v93, v93
	v_pk_fma_f32 v[114:115], v[68:69], v[112:113], v[114:115]
	s_nop 0
	v_mul_f32_e32 v95, 0xbfb8aa3b, v114
	v_exp_f32_e32 v97, v95
	v_mul_f32_e32 v95, 0xbfb8aa3b, v115
	v_exp_f32_e32 v99, v95
	v_pk_fma_f32 v[94:95], v[92:93], v[92:93], v[94:95] op_sel_hi:[1,1,0]
	s_nop 0
	v_add_f32_e32 v95, 1.0, v97
	v_rcp_f32_e32 v120, v95
	v_add_f32_e32 v95, 1.0, v99
	v_rcp_f32_e32 v121, v95
	v_permlane32_swap_b32_e32 v96, v94
	v_add_f32_e32 v107, v96, v94
	v_pk_mul_f32 v[94:95], v[114:115], v[120:121]
	v_pk_mul_f32 v[120:121], v[6:7], v[102:103]
	v_mul_f32_e32 v96, v95, v95
	v_pk_fma_f32 v[100:101], v[4:5], v[100:101], v[120:121]
	v_lshlrev_b32_e32 v114, 16, v125
	v_and_b32_e32 v115, 0xffff0000, v125
	v_pk_fma_f32 v[100:101], v[70:71], v[112:113], v[100:101]
	v_pk_fma_f32 v[96:97], v[94:95], v[94:95], v[96:97] op_sel_hi:[1,1,0]
	v_pk_fma_f32 v[100:101], v[68:69], v[114:115], v[100:101]
	s_nop 0
	v_permlane32_swap_b32_e32 v98, v96
	v_mul_f32_e32 v97, 0xbfb8aa3b, v100
	v_mul_f32_e32 v99, 0xbfb8aa3b, v101
	v_exp_f32_e32 v97, v97
	v_exp_f32_e32 v99, v99
	v_add_f32_e32 v98, v98, v96
	v_pk_mul_f32 v[120:121], v[6:7], v[112:113]
	v_add_f32_e32 v96, 1.0, v97
	v_add_f32_e32 v97, 1.0, v99
	v_rcp_f32_e32 v96, v96
	v_rcp_f32_e32 v97, v97
	v_permlane16_swap_b32_e32 v9, v98
	v_pk_fma_f32 v[102:103], v[4:5], v[102:103], v[120:121]
	v_pk_mul_f32 v[96:97], v[100:101], v[96:97]
	v_add_f32_e32 v9, v9, v98
	v_mul_f32_e32 v98, v97, v97
	v_lshlrev_b32_e32 v100, 16, v126
	v_and_b32_e32 v101, 0xffff0000, v126
	v_pk_fma_f32 v[102:103], v[70:71], v[114:115], v[102:103]
	v_pk_fma_f32 v[98:99], v[96:97], v[96:97], v[98:99] op_sel_hi:[1,1,0]
; DI unsigned pk2(float lo, float hi) { f32x2 v = {lo, hi}; bf16x2_t b = __builtin_convertvector(v, bf16x2_t); return __builtin_bit_cast(unsigned, b); }
; DI float dpp_xor8(float v) { return __uint_as_float((unsigned)__builtin_amdgcn_update_dpp(0, (int)__float_as_uint(v), 0x128, 0xF, 0xF, true)); }
; DI float swap32sum(float a, float b) { const auto r = __builtin_amdgcn_permlane32_swap(__float_as_uint(a), __float_as_uint(b), false, false); return __uint_as_float(r[0]) + __uint_as_float(r[1]); }
; DI float swap16sum(float a, float b) { const auto r = __builtin_amdgcn_permlane16_swap(__float_as_uint(a), __float_as_uint(b), false, false); return __uint_as_float(r[0]) + __uint_as_float(r[1]); }
; DI void gdn_prep_unit(const Params& p, int U, char* lds) {
;     ...
;         for (int j = 0; j < 8; ++j) r8[j] = swap32sum(ssr[j], ssr[8 + j]);
; #pragma unroll
;         for (int j = 0; j < 4; ++j) r4[j] = swap16sum(r8[j], r8[4 + j]);
; #pragma unroll
;         for (int j = 0; j < 2; ++j) { const float keep = b3 ? r4[2 + j] : r4[j], send = b3 ? r4[j] : r4[2 + j]; r2[j] = keep + dpp_xor8(send); }
;         float r1 = (b2 ? r2[1] : r2[0]) + __shfl_xor(b2 ? r2[0] : r2[1], 4);
;         r1 += __uint_as_float((unsigned)__builtin_amdgcn_update_dpp(0, (int)__float_as_uint(r1), 0x4E, 0xF, 0xF, true));
;         r1 += __uint_as_float((unsigned)__builtin_amdgcn_update_dpp(0, (int)__float_as_uint(r1), 0xB1, 0xF, 0xF, true));
; #pragma unroll
;         for (int ii = 0; ii < 16; ++ii) ssr[ii] = __uint_as_float((unsigned)__builtin_amdgcn_readlane((int)__float_as_uint(r1), 4 * ii));
;       }
; #pragma unroll
;       for (int ii = 0; ii < 16; ++ii) {
;         const int i = i0 + ii;
;         float a0 = y0[ii], a1 = y1[ii];
;         if (X < 2) { const float rn = rsqrtf(ssr[ii] + 1e-6f); a0 *= rn; a1 *= rn; }
;         *(unsigned*)(dst + i * QP + 2 * lane) = pk2(a0, a1);
	v_pk_fma_f32 v[102:103], v[68:69], v[100:101], v[102:103]
	s_nop 0
	v_permlane32_swap_b32_e32 v106, v98
	v_mul_f32_e32 v99, 0xbfb8aa3b, v102
	v_mul_f32_e32 v109, 0xbfb8aa3b, v103
	v_exp_f32_e32 v99, v99
	v_exp_f32_e32 v109, v109
	v_add_f32_e32 v106, v106, v98
	v_pk_mul_f32 v[6:7], v[6:7], v[114:115]
	v_add_f32_e32 v98, 1.0, v99
	v_add_f32_e32 v99, 1.0, v109
	v_rcp_f32_e32 v98, v98
	v_rcp_f32_e32 v99, v99
	v_permlane16_swap_b32_e32 v37, v106
	v_pk_fma_f32 v[4:5], v[4:5], v[112:113], v[6:7]
	v_pk_mul_f32 v[98:99], v[102:103], v[98:99]
	v_add_f32_e32 v37, v37, v106
	v_mul_f32_e32 v102, v99, v99
	v_pk_fma_f32 v[102:103], v[98:99], v[98:99], v[102:103] op_sel_hi:[1,1,0]
	v_pk_fma_f32 v[4:5], v[70:71], v[100:101], v[4:5]
	s_nop 0
	v_permlane32_swap_b32_e32 v108, v102
	v_add_f32_e32 v106, v108, v102
	v_lshlrev_b32_e32 v102, 16, v127
	v_and_b32_e32 v103, 0xffff0000, v127
	v_pk_fma_f32 v[4:5], v[68:69], v[102:103], v[4:5]
	v_permlane16_swap_b32_e32 v104, v106
	v_mul_f32_e32 v6, 0xbfb8aa3b, v4
	v_mul_f32_e32 v7, 0xbfb8aa3b, v5
	v_exp_f32_e32 v6, v6
	v_exp_f32_e32 v7, v7
	v_add_f32_e32 v68, v104, v106
	v_cndmask_b32_e64 v69, v68, v9, s[0:1]
	v_add_f32_e32 v6, 1.0, v6
	v_add_f32_e32 v7, 1.0, v7
	v_rcp_f32_e32 v6, v6
	v_rcp_f32_e32 v7, v7
	v_cndmask_b32_e64 v9, v9, v68, s[0:1]
	s_nop 1
	v_add_f32_dpp v9, v9, v69 row_ror:8 row_mask:0xf bank_mask:0xf bound_ctrl:1
	v_pk_mul_f32 v[68:69], v[4:5], v[6:7]
	s_nop 0
	v_mul_f32_e32 v4, v69, v69
	v_pk_fma_f32 v[4:5], v[68:69], v[68:69], v[4:5] op_sel_hi:[1,1,0]
	s_nop 1
	v_permlane32_swap_b32_e32 v118, v4
	v_add_f32_e32 v4, v118, v4
	s_nop 1
	v_permlane16_swap_b32_e32 v107, v4
	v_add_f32_e32 v4, v107, v4
	v_cndmask_b32_e64 v5, v4, v37, s[0:1]
	v_cndmask_b32_e64 v4, v37, v4, s[0:1]
	s_nop 1
	v_add_f32_dpp v4, v4, v5 row_ror:8 row_mask:0xf bank_mask:0xf bound_ctrl:1
	v_cndmask_b32_e64 v5, v9, v4, s[12:13]
	ds_bpermute_b32 v5, v55, v5
	v_cndmask_b32_e64 v4, v4, v9, s[12:13]
	v_and_b32_e32 v55, 15, v175
	s_waitcnt lgkmcnt(0)
	v_add_f32_e32 v4, v4, v5
	s_nop 1
	v_add_f32_dpp v4, v4, v4 quad_perm:[2,3,0,1] row_mask:0xf bank_mask:0xf bound_ctrl:1
	s_nop 1
	v_add_f32_dpp v6, v4, v4 quad_perm:[1,0,3,2] row_mask:0xf bank_mask:0xf bound_ctrl:1
	s_nop 0
	v_readlane_b32 s1, v6, 0
	v_readlane_b32 s0, v6, 4
	v_readlane_b32 s13, v6, 8
	v_readlane_b32 s12, v6, 12
	v_pk_add_f32 v[4:5], s[0:1], v[32:33] op_sel_hi:[1,0]
	v_readlane_b32 s75, v6, 16
	v_mul_f32_e32 v7, 0x4b800000, v5
	v_cmp_gt_f32_e64 s[0:1], s19, v5
	v_readlane_b32 s74, v6, 20
	v_readlane_b32 s61, v6, 24
	v_cndmask_b32_e64 v5, v5, v7, s[0:1]
	v_rsq_f32_e32 v5, v5
	v_readlane_b32 s60, v6, 28
	v_readlane_b32 s51, v6, 32
	v_readlane_b32 s50, v6, 36
	v_readlane_b32 s49, v6, 40
	v_readlane_b32 s48, v6, 44
	v_readlane_b32 s45, v6, 48
	v_readlane_b32 s44, v6, 52
	v_readlane_b32 s15, v6, 56
	v_readlane_b32 s14, v6, 60
	v_mul_f32_e32 v6, 0x45800000, v5
	v_cndmask_b32_e64 v6, v5, v6, s[0:1]
	v_mul_f32_e32 v5, 0x4b800000, v4
	v_cmp_gt_f32_e64 s[0:1], s19, v4
	s_nop 1
	v_cndmask_b32_e64 v4, v4, v5, s[0:1]
	v_rsq_f32_e32 v7, v4
	s_nop 0
	v_pk_mul_f32 v[4:5], v[6:7], v[66:67] op_sel_hi:[0,1]
	v_cvt_pk_bf16_f32 v4, v4, v5
	ds_write_b32 v8, v4 offset:17408
	v_pk_add_f32 v[4:5], s[12:13], v[32:33] op_sel_hi:[1,0]
	v_mul_f32_e32 v6, 0x45800000, v7
	v_mul_f32_e32 v9, 0x4b800000, v5
	v_cmp_gt_f32_e64 s[12:13], s19, v5
	v_cndmask_b32_e64 v6, v7, v6, s[0:1]
	v_pk_mul_f32 v[6:7], v[6:7], v[72:73] op_sel_hi:[0,1]
	v_cndmask_b32_e64 v5, v5, v9, s[12:13]
	v_rsq_f32_e32 v5, v5
	v_cvt_pk_bf16_f32 v9, v6, v7
	v_cmp_gt_f32_e64 s[0:1], s19, v4
	v_add_u32_e32 v66, 0x4400, v36
	v_mul_f32_e32 v6, 0x45800000, v5
	v_cndmask_b32_e64 v6, v5, v6, s[12:13]
	v_mul_f32_e32 v5, 0x4b800000, v4
	v_pk_mul_f32 v[6:7], v[6:7], v[74:75] op_sel_hi:[0,1]
	v_cndmask_b32_e64 v4, v4, v5, s[0:1]
	v_rsq_f32_e32 v37, v4
	v_cvt_pk_bf16_f32 v4, v6, v7
	ds_write2_b32 v66, v9, v4 offset1:68
	v_pk_add_f32 v[4:5], s[74:75], v[32:33] op_sel_hi:[1,0]
	v_mul_f32_e32 v6, 0x45800000, v37
	v_mul_f32_e32 v7, 0x4b800000, v5
	v_cmp_gt_f32_e64 s[12:13], s19, v5
	v_cndmask_b32_e64 v6, v37, v6, s[0:1]
	v_cmp_gt_f32_e64 s[0:1], s19, v4
	v_cndmask_b32_e64 v5, v5, v7, s[12:13]
	v_rsq_f32_e32 v5, v5
	v_pk_mul_f32 v[6:7], v[6:7], v[78:79] op_sel_hi:[0,1]
	v_cvt_pk_bf16_f32 v7, v6, v7
	v_mul_f32_e32 v6, 0x45800000, v5
	v_cndmask_b32_e64 v6, v5, v6, s[12:13]
	v_mul_f32_e32 v5, 0x4b800000, v4
	v_cndmask_b32_e64 v4, v4, v5, s[0:1]
	v_rsq_f32_e32 v9, v4
	v_pk_mul_f32 v[4:5], v[6:7], v[76:77] op_sel_hi:[0,1]
	v_cvt_pk_bf16_f32 v4, v4, v5
	ds_write2_b32 v66, v7, v4 offset0:136 offset1:204
	v_pk_add_f32 v[4:5], s[60:61], v[32:33] op_sel_hi:[1,0]
	v_mul_f32_e32 v6, 0x45800000, v9
	v_mul_f32_e32 v7, 0x4b800000, v5
	v_cmp_gt_f32_e64 s[12:13], s19, v5
	v_cndmask_b32_e64 v6, v9, v6, s[0:1]
	v_cmp_gt_f32_e64 s[0:1], s19, v4
	v_cndmask_b32_e64 v5, v5, v7, s[12:13]
	v_rsq_f32_e32 v5, v5
	v_pk_mul_f32 v[6:7], v[6:7], v[80:81] op_sel_hi:[0,1]
	v_cvt_pk_bf16_f32 v9, v6, v7
	v_add_u32_e32 v66, 0x4800, v36
	v_mul_f32_e32 v6, 0x45800000, v5
	v_cndmask_b32_e64 v6, v5, v6, s[12:13]
	v_mul_f32_e32 v5, 0x4b800000, v4
	v_pk_mul_f32 v[6:7], v[6:7], v[82:83] op_sel_hi:[0,1]
	v_cndmask_b32_e64 v4, v4, v5, s[0:1]
	v_rsq_f32_e32 v37, v4
	v_cvt_pk_bf16_f32 v4, v6, v7
	ds_write2_b32 v66, v9, v4 offset0:16 offset1:84
	v_pk_add_f32 v[4:5], s[50:51], v[32:33] op_sel_hi:[1,0]
	v_mul_f32_e32 v6, 0x45800000, v37
	v_mul_f32_e32 v7, 0x4b800000, v5
	v_cmp_gt_f32_e64 s[12:13], s19, v5
	v_cndmask_b32_e64 v6, v37, v6, s[0:1]
	v_cmp_gt_f32_e64 s[0:1], s19, v4
	v_cndmask_b32_e64 v5, v5, v7, s[12:13]
	v_rsq_f32_e32 v5, v5
	v_pk_mul_f32 v[6:7], v[6:7], v[86:87] op_sel_hi:[0,1]
; DI void gdn_prep_unit(const Params& p, int U, char* lds) {
;     ...
;       for (int j = 0; j < 4; ++j) { w0[j] = p.conv_w[j * 1536 + cb]; w1[j] = p.conv_w[j * 1536 + cb + 1]; }
;       bf16_t* dst = X == 0 ? q_s : (X == 1 ? k_s : v_s);
;       const int i0 = 16 * wid;
;       unsigned raw[19];
;       {
;         const unsigned* pr[19];
; #pragma unroll
;         for (int j = 0; j < 19; ++j) { const int rr = i0 - 3 + j; const int rc = (s0 + rr >= 0) ? rr : -s0;
;           pr[j] = (const unsigned*)(proj + (size_t)((long)t0 + rc) * PP + col); }
;         asm volatile("global_load_dword %0, %10, off\n\tglobal_load_dword %1, %11, off\n\tglobal_load_dword %2, %12, off\n\tglobal_load_dword %3, %13, off\n\tglobal_load_dword %4, %14, off\n\t"
;                      "global_load_dword %5, %15, off\n\tglobal_load_dword %6, %16, off\n\tglobal_load_dword %7, %17, off\n\tglobal_load_dword %8, %18, off\n\tglobal_load_dword %9, %19, off\n\ts_waitcnt vmcnt(0)"
;                      : "=&v"(raw[0]), "=&v"(raw[1]), "=&v"(raw[2]), "=&v"(raw[3]), "=&v"(raw[4]), "=&v"(raw[5]), "=&v"(raw[6]), "=&v"(raw[7]), "=&v"(raw[8]), "=&v"(raw[9])
;                      : "v"(pr[0]), "v"(pr[1]), "v"(pr[2]), "v"(pr[3]), "v"(pr[4]), "v"(pr[5]), "v"(pr[6]), "v"(pr[7]), "v"(pr[8]), "v"(pr[9]) : "memory");
;         asm volatile("global_load_dword %0, %9, off\n\tglobal_load_dword %1, %10, off\n\tglobal_load_dword %2, %11, off\n\tglobal_load_dword %3, %12, off\n\tglobal_load_dword %4, %13, off\n\t"
;                      "global_load_dword %5, %14, off\n\tglobal_load_dword %6, %15, off\n\tglobal_load_dword %7, %16, off\n\tglobal_load_dword %8, %17, off\n\ts_waitcnt vmcnt(0)"
;                      : "=&v"(raw[10]), "=&v"(raw[11]), "=&v"(raw[12]), "=&v"(raw[13]), "=&v"(raw[14]), "=&v"(raw[15]), "=&v"(raw[16]), "=&v"(raw[17]), "=&v"(raw[18])
;                      : "v"(pr[10]), "v"(pr[11]), "v"(pr[12]), "v"(pr[13]), "v"(pr[14]), "v"(pr[15]), "v"(pr[16]), "v"(pr[17]), "v"(pr[18]) : "memory");
; #pragma unroll
;         for (int j = 0; j < 3; ++j) if (s0 + i0 - 3 + j < 0) raw[j] = 0u;
;     ...
;       for (int ii = 0; ii < 16; ++ii) {
;         const int i = i0 + ii;
;         float a0 = y0[ii], a1 = y1[ii];
;         if (X < 2) { const float rn = rsqrtf(ssr[ii] + 1e-6f); a0 *= rn; a1 *= rn; }
;         *(unsigned*)(dst + i * QP + 2 * lane) = pk2(a0, a1);
	v_cvt_pk_bf16_f32 v7, v6, v7
	v_mul_f32_e32 v6, 0x45800000, v5
	v_cndmask_b32_e64 v6, v5, v6, s[12:13]
	v_mul_f32_e32 v5, 0x4b800000, v4
	v_cndmask_b32_e64 v4, v4, v5, s[0:1]
	v_rsq_f32_e32 v9, v4
	v_pk_mul_f32 v[4:5], v[6:7], v[84:85] op_sel_hi:[0,1]
	v_cvt_pk_bf16_f32 v4, v4, v5
	ds_write2_b32 v66, v7, v4 offset0:152 offset1:220
	v_pk_add_f32 v[4:5], s[48:49], v[32:33] op_sel_hi:[1,0]
	v_mul_f32_e32 v6, 0x45800000, v9
	v_mul_f32_e32 v7, 0x4b800000, v5
	v_cmp_gt_f32_e64 s[12:13], s19, v5
	v_cndmask_b32_e64 v6, v9, v6, s[0:1]
	v_cmp_gt_f32_e64 s[0:1], s19, v4
	v_cndmask_b32_e64 v5, v5, v7, s[12:13]
	v_rsq_f32_e32 v5, v5
	v_pk_mul_f32 v[6:7], v[6:7], v[88:89] op_sel_hi:[0,1]
	v_cvt_pk_bf16_f32 v9, v6, v7
	v_add_u32_e32 v66, 0x4c00, v36
	v_mul_f32_e32 v6, 0x45800000, v5
	v_cndmask_b32_e64 v6, v5, v6, s[12:13]
	v_mul_f32_e32 v5, 0x4b800000, v4
	v_pk_mul_f32 v[6:7], v[6:7], v[90:91] op_sel_hi:[0,1]
	v_cndmask_b32_e64 v4, v4, v5, s[0:1]
	v_rsq_f32_e32 v37, v4
	v_cvt_pk_bf16_f32 v4, v6, v7
	ds_write2_b32 v66, v9, v4 offset0:32 offset1:100
	v_pk_add_f32 v[4:5], s[44:45], v[32:33] op_sel_hi:[1,0]
	v_mul_f32_e32 v6, 0x45800000, v37
	v_mul_f32_e32 v7, 0x4b800000, v5
	v_cmp_gt_f32_e64 s[12:13], s19, v5
	v_cndmask_b32_e64 v6, v37, v6, s[0:1]
	v_cmp_gt_f32_e64 s[0:1], s19, v4
	v_cndmask_b32_e64 v5, v5, v7, s[12:13]
	v_rsq_f32_e32 v5, v5
	v_pk_mul_f32 v[6:7], v[6:7], v[92:93] op_sel_hi:[0,1]
	v_cvt_pk_bf16_f32 v7, v6, v7
	v_mul_f32_e32 v6, 0x45800000, v5
	v_cndmask_b32_e64 v6, v5, v6, s[12:13]
	v_mul_f32_e32 v5, 0x4b800000, v4
	v_cndmask_b32_e64 v4, v4, v5, s[0:1]
	v_rsq_f32_e32 v9, v4
	v_pk_mul_f32 v[4:5], v[94:95], v[6:7] op_sel_hi:[1,0]
	v_mul_f32_e32 v6, 0x45800000, v9
	v_cvt_pk_bf16_f32 v4, v4, v5
	ds_write2_b32 v66, v7, v4 offset0:168 offset1:236
	v_pk_add_f32 v[4:5], s[14:15], v[32:33] op_sel_hi:[1,0]
	v_cndmask_b32_e64 v6, v9, v6, s[0:1]
	v_mul_f32_e32 v7, 0x4b800000, v5
	v_cmp_gt_f32_e64 s[12:13], s19, v5
	v_cmp_gt_f32_e64 s[0:1], s19, v4
	s_nop 0
	v_cndmask_b32_e64 v5, v5, v7, s[12:13]
	v_rsq_f32_e32 v5, v5
	v_pk_mul_f32 v[6:7], v[96:97], v[6:7] op_sel_hi:[1,0]
	s_nop 0
	v_cvt_pk_bf16_f32 v9, v6, v7
	v_mul_f32_e32 v6, 0x45800000, v5
	v_cndmask_b32_e64 v6, v5, v6, s[12:13]
	v_pk_mul_f32 v[6:7], v[98:99], v[6:7] op_sel_hi:[1,0]
	v_mul_f32_e32 v5, 0x4b800000, v4
	v_cvt_pk_bf16_f32 v6, v6, v7
	v_cndmask_b32_e64 v7, v4, v5, s[0:1]
	global_load_dwordx2 v[4:5], v[64:65], off
	s_nop 0
	global_load_dwordx2 v[2:3], v[2:3], off offset:2048
	v_rsq_f32_e32 v37, v7
	v_add_u32_e32 v7, 0x5000, v36
	ds_write2_b32 v7, v9, v6 offset0:48 offset1:116
	global_load_dwordx2 v[6:7], v[56:57], off
	v_mul_f32_e32 v9, 0x45800000, v37
	global_load_dwordx2 v[0:1], v[0:1], off offset:2048
	v_cndmask_b32_e64 v56, v37, v9, s[0:1]
	s_mov_b64 s[0:1], 0x1400
	v_pk_mul_f32 v[56:57], v[68:69], v[56:57] op_sel_hi:[1,0]
	v_lshl_add_u64 v[10:11], v[10:11], 0, s[0:1]
	v_cvt_pk_bf16_f32 v9, v56, v57
	v_mad_u64_u32 v[56:57], s[0:1], v12, s3, v[10:11]
	v_add_u32_e32 v57, v13, v57
	v_mad_u64_u32 v[12:13], s[0:1], v14, s3, v[10:11]
	v_add_u32_e32 v13, v15, v13
	v_mad_u64_u32 v[14:15], s[0:1], v16, s3, v[10:11]
	v_add_u32_e32 v15, v17, v15
	v_mad_u64_u32 v[16:17], s[0:1], v18, s3, v[10:11]
	v_add_u32_e32 v17, v19, v17
	v_mad_u64_u32 v[18:19], s[0:1], v20, s3, v[10:11]
	v_add_u32_e32 v19, v21, v19
	v_mad_u64_u32 v[20:21], s[0:1], v22, s3, v[10:11]
	v_add_u32_e32 v21, v23, v21
	v_mad_u64_u32 v[22:23], s[0:1], v24, s3, v[10:11]
	v_add_u32_e32 v23, v25, v23
	v_mad_u64_u32 v[24:25], s[0:1], v38, s3, v[10:11]
	ds_write_b32 v36, v9 offset:21216
	v_add_u32_e32 v25, v39, v25
	v_mad_u64_u32 v[38:39], s[0:1], v40, s3, v[10:11]
	v_mad_u64_u32 v[64:65], s[0:1], v42, s3, v[10:11]
	v_mad_u64_u32 v[66:67], s[0:1], v44, s3, v[10:11]
	v_mad_u64_u32 v[76:77], s[0:1], v58, s3, v[10:11]
	v_add_u32_e32 v39, v193, v39
	v_add_u32_e32 v65, v194, v65
	v_add_u32_e32 v67, v45, v67
	v_mad_u64_u32 v[44:45], s[0:1], v46, s3, v[10:11]
	v_mad_u64_u32 v[68:69], s[0:1], v48, s3, v[10:11]
	v_mad_u64_u32 v[70:71], s[0:1], v50, s3, v[10:11]
	v_mad_u64_u32 v[72:73], s[0:1], v52, s3, v[10:11]
	v_mad_u64_u32 v[74:75], s[0:1], v54, s3, v[10:11]
	v_add_u32_e32 v77, v59, v77
	v_mad_u64_u32 v[58:59], s[0:1], v60, s3, v[10:11]
	global_load_dword v9, v[56:57], off
	global_load_dword v37, v[12:13], off
	global_load_dword v40, v[14:15], off
	global_load_dword v42, v[16:17], off
	global_load_dword v46, v[18:19], off
	global_load_dword v48, v[20:21], off
	global_load_dword v50, v[22:23], off
	global_load_dword v52, v[24:25], off
	global_load_dword v54, v[38:39], off
	global_load_dword v60, v[64:65], off
	s_waitcnt vmcnt(0)
	v_mad_u64_u32 v[10:11], s[0:1], v62, s3, v[10:11]
	v_cndmask_b32_e64 v15, v37, 0, s[8:9]
	v_cndmask_b32_e64 v9, v9, 0, vcc
	v_lshlrev_b32_e32 v14, 16, v15
	v_and_b32_e32 v15, 0xffff0000, v15
	v_cndmask_b32_e64 v18, v40, 0, s[10:11]
	v_lshlrev_b32_e32 v12, 16, v9
	v_and_b32_e32 v13, 0xffff0000, v9
	v_and_b32_e32 v19, 0xffff0000, v42
	v_add_u32_e32 v45, v195, v45
	v_add_u32_e32 v69, v196, v69
	v_add_u32_e32 v71, v197, v71
	v_add_u32_e32 v73, v198, v73
	v_add_u32_e32 v75, v199, v75
	v_add_u32_e32 v59, v61, v59
	v_add_u32_e32 v11, v63, v11
	v_cmp_gt_i32_e32 vcc, 1, v181
	s_waitcnt vmcnt(2)
	v_pk_mul_f32 v[16:17], v[2:3], v[14:15]
	s_nop 0
	v_pk_fma_f32 v[12:13], v[4:5], v[12:13], v[16:17]
	v_lshlrev_b32_e32 v16, 16, v18
	v_and_b32_e32 v17, 0xffff0000, v18
	s_waitcnt vmcnt(1)
	v_pk_fma_f32 v[12:13], v[6:7], v[16:17], v[12:13]
	v_lshlrev_b32_e32 v18, 16, v42
	s_waitcnt vmcnt(0)
; DI float bflo(unsigned u) { return __uint_as_float(u << 16); }
; DI float bfhi(unsigned u) { return __uint_as_float(u & 0xffff0000u); }
; DI float sigmoidf_(float x) { return __builtin_amdgcn_rcpf(1.f + __expf(-x)); }
; DI void gdn_prep_unit(const Params& p, int U, char* lds) {
;     ...
;         asm volatile("global_load_dword %0, %9, off\n\tglobal_load_dword %1, %10, off\n\tglobal_load_dword %2, %11, off\n\tglobal_load_dword %3, %12, off\n\tglobal_load_dword %4, %13, off\n\t"
;                      "global_load_dword %5, %14, off\n\tglobal_load_dword %6, %15, off\n\tglobal_load_dword %7, %16, off\n\tglobal_load_dword %8, %17, off\n\ts_waitcnt vmcnt(0)"
;                      : "=&v"(raw[10]), "=&v"(raw[11]), "=&v"(raw[12]), "=&v"(raw[13]), "=&v"(raw[14]), "=&v"(raw[15]), "=&v"(raw[16]), "=&v"(raw[17]), "=&v"(raw[18])
;                      : "v"(pr[10]), "v"(pr[11]), "v"(pr[12]), "v"(pr[13]), "v"(pr[14]), "v"(pr[15]), "v"(pr[16]), "v"(pr[17]), "v"(pr[18]) : "memory");
; #pragma unroll
;         for (int j = 0; j < 3; ++j) if (s0 + i0 - 3 + j < 0) raw[j] = 0u;
;       }
;       float y0[16], y1[16], ssr[16];
; #pragma unroll
;       for (int ii = 0; ii < 16; ++ii) {
;         float a0 = w0[0] * bflo(raw[ii]) + w0[1] * bflo(raw[ii + 1]) + w0[2] * bflo(raw[ii + 2]) + w0[3] * bflo(raw[ii + 3]);
;         float a1 = w1[0] * bfhi(raw[ii]) + w1[1] * bfhi(raw[ii + 1]) + w1[2] * bfhi(raw[ii + 2]) + w1[3] * bfhi(raw[ii + 3]);
;         a0 = a0 * sigmoidf_(a0); a1 = a1 * sigmoidf_(a1);
;         y0[ii] = a0; y1[ii] = a1; ssr[ii] = a0 * a0 + a1 * a1;
	v_pk_fma_f32 v[12:13], v[0:1], v[18:19], v[12:13]
	global_load_dword v37, v[66:67], off
	global_load_dword v40, v[44:45], off
	global_load_dword v42, v[68:69], off
	global_load_dword v78, v[70:71], off
	global_load_dword v79, v[72:73], off
	global_load_dword v80, v[74:75], off
	global_load_dword v81, v[76:77], off
	global_load_dword v82, v[58:59], off
	global_load_dword v83, v[10:11], off
	s_waitcnt vmcnt(0)
	s_nop 0
	v_mul_f32_e32 v9, 0xbfb8aa3b, v12
	v_exp_f32_e32 v9, v9
	v_mul_f32_e32 v20, 0xbfb8aa3b, v13
	v_exp_f32_e32 v20, v20
	v_add_f32_e32 v9, 1.0, v9
	v_rcp_f32_e32 v10, v9
	v_add_f32_e32 v9, 1.0, v20
	v_pk_mul_f32 v[20:21], v[2:3], v[16:17]
	v_rcp_f32_e32 v11, v9
	v_pk_fma_f32 v[14:15], v[4:5], v[14:15], v[20:21]
	v_lshlrev_b32_e32 v20, 16, v46
	v_pk_fma_f32 v[14:15], v[6:7], v[18:19], v[14:15]
	v_and_b32_e32 v21, 0xffff0000, v46
	v_pk_fma_f32 v[14:15], v[0:1], v[20:21], v[14:15]
	v_pk_mul_f32 v[10:11], v[12:13], v[10:11]
	v_mul_f32_e32 v9, 0xbfb8aa3b, v14
	v_exp_f32_e32 v9, v9
	v_mul_f32_e32 v22, 0xbfb8aa3b, v15
	v_exp_f32_e32 v22, v22
	v_add_f32_e32 v9, 1.0, v9
	v_rcp_f32_e32 v12, v9
	v_add_f32_e32 v9, 1.0, v22
	v_pk_mul_f32 v[22:23], v[2:3], v[18:19]
	v_rcp_f32_e32 v13, v9
	v_pk_fma_f32 v[16:17], v[4:5], v[16:17], v[22:23]
	v_lshlrev_b32_e32 v22, 16, v48
	v_pk_fma_f32 v[16:17], v[6:7], v[20:21], v[16:17]
	v_and_b32_e32 v23, 0xffff0000, v48
	v_pk_fma_f32 v[16:17], v[0:1], v[22:23], v[16:17]
	v_pk_mul_f32 v[12:13], v[14:15], v[12:13]
	v_mul_f32_e32 v9, 0xbfb8aa3b, v16
	v_exp_f32_e32 v9, v9
	v_mul_f32_e32 v24, 0xbfb8aa3b, v17
	v_exp_f32_e32 v24, v24
	v_add_f32_e32 v9, 1.0, v9
	v_rcp_f32_e32 v14, v9
	v_add_f32_e32 v9, 1.0, v24
	v_pk_mul_f32 v[24:25], v[2:3], v[20:21]
	v_rcp_f32_e32 v15, v9
	v_pk_fma_f32 v[18:19], v[4:5], v[18:19], v[24:25]
	v_lshlrev_b32_e32 v24, 16, v50
	v_pk_fma_f32 v[18:19], v[6:7], v[22:23], v[18:19]
	v_and_b32_e32 v25, 0xffff0000, v50
	v_pk_fma_f32 v[18:19], v[0:1], v[24:25], v[18:19]
	v_pk_mul_f32 v[14:15], v[16:17], v[14:15]
	v_mul_f32_e32 v9, 0xbfb8aa3b, v18
	v_exp_f32_e32 v9, v9
	v_mul_f32_e32 v38, 0xbfb8aa3b, v19
	v_exp_f32_e32 v38, v38
	v_add_f32_e32 v9, 1.0, v9
	v_rcp_f32_e32 v16, v9
	v_add_f32_e32 v9, 1.0, v38
	v_pk_mul_f32 v[38:39], v[2:3], v[22:23]
	v_rcp_f32_e32 v17, v9
	v_pk_fma_f32 v[20:21], v[4:5], v[20:21], v[38:39]
	v_lshlrev_b32_e32 v38, 16, v52
	v_pk_fma_f32 v[20:21], v[6:7], v[24:25], v[20:21]
	v_and_b32_e32 v39, 0xffff0000, v52
	v_pk_fma_f32 v[20:21], v[0:1], v[38:39], v[20:21]
	v_pk_mul_f32 v[16:17], v[18:19], v[16:17]
	v_mul_f32_e32 v9, 0xbfb8aa3b, v20
	v_exp_f32_e32 v9, v9
	v_mul_f32_e32 v44, 0xbfb8aa3b, v21
	v_exp_f32_e32 v44, v44
	v_pk_mul_f32 v[56:57], v[2:3], v[38:39]
	v_add_f32_e32 v9, 1.0, v9
	v_rcp_f32_e32 v18, v9
	v_add_f32_e32 v9, 1.0, v44
	v_pk_mul_f32 v[44:45], v[2:3], v[24:25]
	v_rcp_f32_e32 v19, v9
	v_pk_fma_f32 v[22:23], v[4:5], v[22:23], v[44:45]
	v_lshlrev_b32_e32 v44, 16, v54
	v_pk_fma_f32 v[22:23], v[6:7], v[38:39], v[22:23]
	v_and_b32_e32 v45, 0xffff0000, v54
	v_pk_fma_f32 v[22:23], v[0:1], v[44:45], v[22:23]
	v_pk_fma_f32 v[24:25], v[4:5], v[24:25], v[56:57]
	v_mul_f32_e32 v9, 0xbfb8aa3b, v22
	v_exp_f32_e32 v9, v9
	v_mul_f32_e32 v46, 0xbfb8aa3b, v23
	v_exp_f32_e32 v46, v46
	v_pk_fma_f32 v[24:25], v[6:7], v[44:45], v[24:25]
	v_add_f32_e32 v9, 1.0, v9
	v_lshlrev_b32_e32 v56, 16, v60
	v_and_b32_e32 v57, 0xffff0000, v60
	v_pk_mul_f32 v[18:19], v[20:21], v[18:19]
	v_rcp_f32_e32 v20, v9
	v_add_f32_e32 v9, 1.0, v46
	v_pk_fma_f32 v[24:25], v[0:1], v[56:57], v[24:25]
	v_rcp_f32_e32 v21, v9
	v_mul_f32_e32 v9, 0xbfb8aa3b, v24
	v_exp_f32_e32 v9, v9
	v_mul_f32_e32 v46, 0xbfb8aa3b, v25
	v_exp_f32_e32 v46, v46
	v_pk_mul_f32 v[58:59], v[2:3], v[44:45]
	v_add_f32_e32 v9, 1.0, v9
	v_pk_fma_f32 v[38:39], v[4:5], v[38:39], v[58:59]
	v_lshlrev_b32_e32 v58, 16, v37
	v_pk_fma_f32 v[38:39], v[6:7], v[56:57], v[38:39]
	v_and_b32_e32 v59, 0xffff0000, v37
	v_pk_mul_f32 v[20:21], v[22:23], v[20:21]
	v_rcp_f32_e32 v22, v9
	v_add_f32_e32 v9, 1.0, v46
	v_pk_fma_f32 v[38:39], v[0:1], v[58:59], v[38:39]
	v_rcp_f32_e32 v23, v9
	v_mul_f32_e32 v9, 0xbfb8aa3b, v38
	v_exp_f32_e32 v9, v9
	v_mul_f32_e32 v37, 0xbfb8aa3b, v39
	v_exp_f32_e32 v37, v37
	v_pk_mul_f32 v[60:61], v[2:3], v[56:57]
	v_add_f32_e32 v9, 1.0, v9
	v_pk_fma_f32 v[44:45], v[4:5], v[44:45], v[60:61]
	v_lshlrev_b32_e32 v60, 16, v40
	v_pk_fma_f32 v[44:45], v[6:7], v[58:59], v[44:45]
	v_and_b32_e32 v61, 0xffff0000, v40
	v_pk_mul_f32 v[22:23], v[24:25], v[22:23]
	v_rcp_f32_e32 v24, v9
	v_add_f32_e32 v9, 1.0, v37
	v_pk_fma_f32 v[44:45], v[0:1], v[60:61], v[44:45]
	v_rcp_f32_e32 v25, v9
	v_mul_f32_e32 v9, 0xbfb8aa3b, v44
	v_exp_f32_e32 v9, v9
	v_mul_f32_e32 v37, 0xbfb8aa3b, v45
	v_exp_f32_e32 v37, v37
	v_pk_mul_f32 v[62:63], v[2:3], v[58:59]
	v_add_f32_e32 v9, 1.0, v9
	v_pk_fma_f32 v[56:57], v[4:5], v[56:57], v[62:63]
	v_lshlrev_b32_e32 v62, 16, v42
	v_pk_fma_f32 v[56:57], v[6:7], v[60:61], v[56:57]
	v_and_b32_e32 v63, 0xffff0000, v42
	v_pk_mul_f32 v[24:25], v[38:39], v[24:25]
	v_rcp_f32_e32 v38, v9
	v_add_f32_e32 v9, 1.0, v37
	v_pk_fma_f32 v[56:57], v[0:1], v[62:63], v[56:57]
	v_rcp_f32_e32 v39, v9
	v_mul_f32_e32 v9, 0xbfb8aa3b, v56
	v_exp_f32_e32 v9, v9
	v_mul_f32_e32 v37, 0xbfb8aa3b, v57
	v_exp_f32_e32 v37, v37
	v_pk_mul_f32 v[64:65], v[2:3], v[60:61]
	v_add_f32_e32 v9, 1.0, v9
	v_pk_fma_f32 v[58:59], v[4:5], v[58:59], v[64:65]
	v_lshlrev_b32_e32 v64, 16, v78
	v_pk_fma_f32 v[58:59], v[6:7], v[62:63], v[58:59]
	v_and_b32_e32 v65, 0xffff0000, v78
	v_pk_mul_f32 v[38:39], v[44:45], v[38:39]
	v_rcp_f32_e32 v44, v9
	v_add_f32_e32 v9, 1.0, v37
	v_pk_fma_f32 v[58:59], v[0:1], v[64:65], v[58:59]
; DI unsigned pk2(float lo, float hi) { f32x2 v = {lo, hi}; bf16x2_t b = __builtin_convertvector(v, bf16x2_t); return __builtin_bit_cast(unsigned, b); }
; #define MFMA16(a, b, c) __builtin_amdgcn_mfma_f32_16x16x32_bf16((a), (b), (c), 0, 0, 0)
; DI void gdn_prep_unit(const Params& p, int U, char* lds) {
;     ...
;       for (int ii = 0; ii < 16; ++ii) {
;         const int i = i0 + ii;
;         float a0 = y0[ii], a1 = y1[ii];
;         if (X < 2) { const float rn = rsqrtf(ssr[ii] + 1e-6f); a0 *= rn; a1 *= rn; }
;         *(unsigned*)(dst + i * QP + 2 * lane) = pk2(a0, a1);
;     ...
;   __syncthreads();
;   {
;     bf16x8 ka[4];
; #pragma unroll
;     for (int kk = 0; kk < 4; ++kk) ka[kk] = *(const bf16x8*)(k_s + (16 * wid + fr) * QP + kk * 32 + fq * 8);
; #pragma unroll
;     for (int ni = 0; ni < 4; ++ni) {
;       f32x4 dkk = {0.f, 0.f, 0.f, 0.f}, dqk = {0.f, 0.f, 0.f, 0.f};
;       const int i = 16 * ni + fr, jj0 = 16 * wid + 4 * fq;
;       if (ni >= wid) {
; #pragma unroll
;         for (int kk = 0; kk < 4; ++kk) {
;           const bf16x8 bk = *(const bf16x8*)(k_s + (16 * ni + fr) * QP + kk * 32 + fq * 8), bq = *(const bf16x8*)(q_s + (16 * ni + fr) * QP + kk * 32 + fq * 8);
;           dkk = MFMA16(ka[kk], bk, dkk); dqk = MFMA16(ka[kk], bq, dqk);
;         }
;       }
	v_rcp_f32_e32 v45, v9
	v_mul_f32_e32 v9, 0xbfb8aa3b, v58
	v_exp_f32_e32 v9, v9
	v_mul_f32_e32 v37, 0xbfb8aa3b, v59
	v_exp_f32_e32 v37, v37
	v_pk_mul_f32 v[66:67], v[2:3], v[62:63]
	v_add_f32_e32 v9, 1.0, v9
	v_pk_fma_f32 v[60:61], v[4:5], v[60:61], v[66:67]
	v_lshlrev_b32_e32 v66, 16, v79
	v_pk_fma_f32 v[60:61], v[6:7], v[64:65], v[60:61]
	v_and_b32_e32 v67, 0xffff0000, v79
	v_pk_mul_f32 v[44:45], v[56:57], v[44:45]
	v_rcp_f32_e32 v56, v9
	v_add_f32_e32 v9, 1.0, v37
	v_pk_fma_f32 v[60:61], v[0:1], v[66:67], v[60:61]
	v_rcp_f32_e32 v57, v9
	v_mul_f32_e32 v9, 0xbfb8aa3b, v60
	v_exp_f32_e32 v9, v9
	v_mul_f32_e32 v37, 0xbfb8aa3b, v61
	v_exp_f32_e32 v37, v37
	v_pk_mul_f32 v[68:69], v[2:3], v[64:65]
	v_add_f32_e32 v9, 1.0, v9
	v_pk_fma_f32 v[62:63], v[4:5], v[62:63], v[68:69]
	v_lshlrev_b32_e32 v68, 16, v80
	v_pk_fma_f32 v[62:63], v[6:7], v[66:67], v[62:63]
	v_and_b32_e32 v69, 0xffff0000, v80
	v_pk_mul_f32 v[56:57], v[58:59], v[56:57]
	v_rcp_f32_e32 v58, v9
	v_add_f32_e32 v9, 1.0, v37
	v_pk_fma_f32 v[62:63], v[0:1], v[68:69], v[62:63]
	v_rcp_f32_e32 v59, v9
	v_mul_f32_e32 v9, 0xbfb8aa3b, v62
	v_pk_mul_f32 v[70:71], v[2:3], v[66:67]
	v_exp_f32_e32 v9, v9
	v_mul_f32_e32 v37, 0xbfb8aa3b, v63
	v_pk_fma_f32 v[64:65], v[4:5], v[64:65], v[70:71]
	v_lshlrev_b32_e32 v70, 16, v81
	v_and_b32_e32 v71, 0xffff0000, v81
	v_exp_f32_e32 v37, v37
	v_pk_mul_f32 v[74:75], v[2:3], v[68:69]
	v_pk_mul_f32 v[2:3], v[2:3], v[70:71]
	v_pk_fma_f32 v[66:67], v[4:5], v[66:67], v[74:75]
	v_lshlrev_b32_e32 v74, 16, v82
	v_and_b32_e32 v75, 0xffff0000, v82
	v_pk_fma_f32 v[2:3], v[4:5], v[68:69], v[2:3]
	v_pk_fma_f32 v[64:65], v[6:7], v[68:69], v[64:65]
	v_pk_fma_f32 v[66:67], v[6:7], v[70:71], v[66:67]
	v_pk_fma_f32 v[2:3], v[6:7], v[74:75], v[2:3]
	v_lshlrev_b32_e32 v4, 16, v83
	v_and_b32_e32 v5, 0xffff0000, v83
	v_add_f32_e32 v9, 1.0, v9
	v_pk_fma_f32 v[64:65], v[0:1], v[70:71], v[64:65]
	v_pk_fma_f32 v[66:67], v[0:1], v[74:75], v[66:67]
	v_pk_fma_f32 v[0:1], v[0:1], v[4:5], v[2:3]
	v_pk_mul_f32 v[58:59], v[60:61], v[58:59]
	v_rcp_f32_e32 v60, v9
	v_add_f32_e32 v9, 1.0, v37
	v_mul_f32_e32 v37, 0xbfb8aa3b, v64
	v_mul_f32_e32 v2, 0xbfb8aa3b, v0
	v_mul_f32_e32 v3, 0xbfb8aa3b, v1
	v_exp_f32_e32 v37, v37
	v_mul_f32_e32 v40, 0xbfb8aa3b, v65
	v_exp_f32_e32 v2, v2
	v_exp_f32_e32 v3, v3
	v_exp_f32_e32 v40, v40
	v_rcp_f32_e32 v61, v9
	v_add_f32_e32 v9, 1.0, v37
	v_mul_f32_e32 v37, 0xbfb8aa3b, v66
	v_add_f32_e32 v2, 1.0, v2
	v_add_f32_e32 v3, 1.0, v3
	v_rcp_f32_e32 v72, v9
	v_add_f32_e32 v9, 1.0, v40
	v_exp_f32_e32 v37, v37
	v_mul_f32_e32 v40, 0xbfb8aa3b, v67
	v_rcp_f32_e32 v2, v2
	v_rcp_f32_e32 v3, v3
	v_exp_f32_e32 v40, v40
	v_rcp_f32_e32 v73, v9
	v_add_f32_e32 v9, 1.0, v37
	v_pk_mul_f32 v[0:1], v[0:1], v[2:3]
	v_cvt_pk_bf16_f32 v2, v10, v11
	v_rcp_f32_e32 v76, v9
	v_add_f32_e32 v9, 1.0, v40
	ds_write_b32 v8, v2 offset:34816
	v_cvt_pk_bf16_f32 v2, v12, v13
	v_cvt_pk_bf16_f32 v3, v14, v15
	v_add_u32_e32 v8, 0x8800, v36
	v_rcp_f32_e32 v77, v9
	ds_write2_b32 v8, v2, v3 offset1:68
	v_cvt_pk_bf16_f32 v2, v16, v17
	v_cvt_pk_bf16_f32 v3, v18, v19
	ds_write2_b32 v8, v2, v3 offset0:136 offset1:204
	v_cvt_pk_bf16_f32 v2, v20, v21
	v_cvt_pk_bf16_f32 v3, v22, v23
	v_add_u32_e32 v8, 0x8c00, v36
	ds_write2_b32 v8, v2, v3 offset0:16 offset1:84
	v_cvt_pk_bf16_f32 v2, v24, v25
	v_cvt_pk_bf16_f32 v3, v38, v39
	v_pk_mul_f32 v[4:5], v[62:63], v[60:61]
	ds_write2_b32 v8, v2, v3 offset0:152 offset1:220
	v_cvt_pk_bf16_f32 v2, v44, v45
	v_cvt_pk_bf16_f32 v3, v56, v57
	v_add_u32_e32 v8, 0x9000, v36
	v_pk_mul_f32 v[6:7], v[64:65], v[72:73]
	v_pk_mul_f32 v[60:61], v[66:67], v[76:77]
	ds_write2_b32 v8, v2, v3 offset0:32 offset1:100
	v_cvt_pk_bf16_f32 v2, v58, v59
	v_cvt_pk_bf16_f32 v3, v4, v5
	ds_write2_b32 v8, v2, v3 offset0:168 offset1:236
	v_cvt_pk_bf16_f32 v2, v6, v7
	v_cvt_pk_bf16_f32 v3, v60, v61
	v_add_u32_e32 v4, 0x9400, v36
	v_cvt_pk_bf16_f32 v0, v0, v1
	ds_write2_b32 v4, v2, v3 offset0:48 offset1:116
	ds_write_b32 v36, v0 offset:38624
	v_and_b32_e32 v0, 48, v178
	v_or_b32_e32 v46, v27, v55
	v_add_u32_e32 v42, v146, v0
	v_mad_u64_u32 v[0:1], s[0:1], v46, s18, v[42:43]
	s_waitcnt lgkmcnt(0)
	s_barrier
	ds_read_b128 v[12:15], v0 offset:17408
	ds_read_b128 v[8:11], v0 offset:17472
	ds_read_b128 v[4:7], v0 offset:17536
	ds_read_b128 v[0:3], v0 offset:17600
	v_mov_b32_e32 v16, 0
	v_mov_b32_e32 v18, 0
	v_mov_b32_e32 v19, 0
	v_mov_b32_e32 v20, 0
	v_mov_b32_e32 v21, 0
	v_mov_b32_e32 v22, 0
	v_mov_b32_e32 v23, 0
	v_mov_b32_e32 v24, 0
	v_mov_b32_e32 v25, 0
	s_and_saveexec_b64 s[0:1], vcc
	s_cbranch_execz .LBB0_1094
	v_mul_u32_u24_e32 v17, 0x88, v55
	v_lshl_add_u32 v17, v17, 1, v42
	ds_read_b128 v[18:21], v17 offset:17408
	ds_read_b128 v[22:25], v17 offset:17472
	ds_read_b128 v[36:39], v17
	ds_read_b128 v[56:59], v17 offset:64
	s_waitcnt lgkmcnt(3)
	v_mfma_f32_16x16x32_bf16 v[18:21], v[12:15], v[18:21], 0
	s_waitcnt lgkmcnt(1)
	v_mfma_f32_16x16x32_bf16 v[36:39], v[12:15], v[36:39], 0
	v_mfma_f32_16x16x32_bf16 v[18:21], v[8:11], v[22:25], v[18:21]
	s_waitcnt lgkmcnt(0)
	v_mfma_f32_16x16x32_bf16 v[22:25], v[8:11], v[56:59], v[36:39]
	s_nop 4
	ds_read_b128 v[36:39], v17 offset:17536
	ds_read_b128 v[56:59], v17 offset:17600
	s_waitcnt lgkmcnt(1)
	v_mfma_f32_16x16x32_bf16 v[18:21], v[4:7], v[36:39], v[18:21]
	ds_read_b128 v[36:39], v17 offset:128
	ds_read_b128 v[60:63], v17 offset:192
	s_waitcnt lgkmcnt(1)
	v_mfma_f32_16x16x32_bf16 v[36:39], v[4:7], v[36:39], v[22:25]
	v_mfma_f32_16x16x32_bf16 v[22:25], v[0:3], v[56:59], v[18:21]
	s_waitcnt lgkmcnt(0)
	v_mfma_f32_16x16x32_bf16 v[18:21], v[0:3], v[60:63], v[36:39]
